# hot loop heads (GEMM K loops, attention tile loops) aligned to 64 bytes; no other change
# baseline (speedup 1.0000x reference)
.LBB0_1260:
	s_ashr_i32 s19, s18, 31
	s_lshl_b64 s[26:27], s[18:19], 19
	s_add_u32 s40, s54, s26
	s_addc_u32 s41, s55, s27
	s_ashr_i32 s17, s16, 31
	s_lshl_b64 s[26:27], s[16:17], 19
	s_add_u32 s42, s56, s26
	s_addc_u32 s43, s57, s27
	s_and_b64 s[26:27], s[38:39], exec
	s_cselect_b32 s13, s43, s47
	s_cselect_b32 s17, s42, s46
	s_add_u32 s19, s46, 0x100
	s_addc_u32 s25, s47, 0
	s_add_u32 s26, s44, 0x40080
	s_addc_u32 s27, s45, 0
	v_mov_b32_e32 v2, 0
	v_lshl_add_u64 v[132:133], s[26:27], 0, v[164:165]
	v_lshl_add_u64 v[134:135], s[26:27], 0, v[166:167]
	s_mov_b32 s26, -2
	s_mov_b64 s[46:47], 0
	v_mov_b32_e32 v3, v2
	v_mov_b32_e32 v4, v2
	v_mov_b32_e32 v5, v2
	v_mov_b32_e32 v6, v2
	s_waitcnt lgkmcnt(0)
	v_mov_b32_e32 v7, v2
	v_mov_b32_e32 v8, v2
	v_mov_b32_e32 v9, v2
	v_mov_b32_e32 v18, v2
	v_mov_b32_e32 v19, v2
	v_mov_b32_e32 v20, v2
	v_mov_b32_e32 v21, v2
	v_mov_b32_e32 v22, v2
	v_mov_b32_e32 v23, v2
	v_mov_b32_e32 v24, v2
	v_mov_b32_e32 v25, v2
	v_mov_b32_e32 v34, v2
	v_mov_b32_e32 v35, v2
	v_mov_b32_e32 v36, v2
	v_mov_b32_e32 v37, v2
	v_mov_b32_e32 v38, v2
	v_mov_b32_e32 v39, v2
	v_mov_b32_e32 v40, v2
	v_mov_b32_e32 v41, v2
	v_mov_b32_e32 v50, v2
	v_mov_b32_e32 v51, v2
	v_mov_b32_e32 v52, v2
	v_mov_b32_e32 v53, v2
	v_mov_b32_e32 v54, v2
	v_mov_b32_e32 v55, v2
	v_mov_b32_e32 v56, v2
	v_mov_b32_e32 v57, v2
	v_mov_b32_e32 v10, v2
	v_mov_b32_e32 v11, v2
	v_mov_b32_e32 v12, v2
	v_mov_b32_e32 v13, v2
	v_mov_b32_e32 v14, v2
	v_mov_b32_e32 v15, v2
	v_mov_b32_e32 v16, v2
	v_mov_b32_e32 v17, v2
	v_mov_b32_e32 v26, v2
	v_mov_b32_e32 v27, v2
	v_mov_b32_e32 v28, v2
	v_mov_b32_e32 v29, v2
	v_mov_b32_e32 v30, v2
	v_mov_b32_e32 v31, v2
	v_mov_b32_e32 v32, v2
	v_mov_b32_e32 v33, v2
	v_mov_b32_e32 v42, v2
	v_mov_b32_e32 v43, v2
	v_mov_b32_e32 v44, v2
	v_mov_b32_e32 v45, v2
	v_mov_b32_e32 v46, v2
	v_mov_b32_e32 v47, v2
	v_mov_b32_e32 v48, v2
	v_mov_b32_e32 v49, v2
	v_mov_b32_e32 v58, v2
	v_mov_b32_e32 v59, v2
	v_mov_b32_e32 v60, v2
	v_mov_b32_e32 v61, v2
	v_mov_b32_e32 v62, v2
	v_mov_b32_e32 v63, v2
	v_mov_b32_e32 v64, v2
	v_mov_b32_e32 v65, v2
	v_mov_b32_e32 v66, v2
	v_mov_b32_e32 v67, v2
	v_mov_b32_e32 v68, v2
	v_mov_b32_e32 v69, v2
	v_mov_b32_e32 v70, v2
	v_mov_b32_e32 v71, v2
	v_mov_b32_e32 v72, v2
	v_mov_b32_e32 v73, v2
	v_mov_b32_e32 v82, v2
	v_mov_b32_e32 v83, v2
	v_mov_b32_e32 v84, v2
	v_mov_b32_e32 v85, v2
	v_mov_b32_e32 v86, v2
	v_mov_b32_e32 v87, v2
	v_mov_b32_e32 v88, v2
	v_mov_b32_e32 v89, v2
	v_mov_b32_e32 v100, v2
	v_mov_b32_e32 v101, v2
	v_mov_b32_e32 v102, v2
	v_mov_b32_e32 v103, v2
	v_mov_b32_e32 v104, v2
	v_mov_b32_e32 v105, v2
	v_mov_b32_e32 v106, v2
	v_mov_b32_e32 v107, v2
	v_mov_b32_e32 v116, v2
	v_mov_b32_e32 v117, v2
	v_mov_b32_e32 v118, v2
	v_mov_b32_e32 v119, v2
	v_mov_b32_e32 v120, v2
	v_mov_b32_e32 v121, v2
	v_mov_b32_e32 v122, v2
	v_mov_b32_e32 v123, v2
	v_mov_b32_e32 v74, v2
	v_mov_b32_e32 v75, v2
	v_mov_b32_e32 v76, v2
	v_mov_b32_e32 v77, v2
	v_mov_b32_e32 v78, v2
	v_mov_b32_e32 v79, v2
	v_mov_b32_e32 v80, v2
	v_mov_b32_e32 v81, v2
	v_mov_b32_e32 v90, v2
	v_mov_b32_e32 v91, v2
	v_mov_b32_e32 v92, v2
	v_mov_b32_e32 v93, v2
	v_mov_b32_e32 v94, v2
	v_mov_b32_e32 v95, v2
	v_mov_b32_e32 v96, v2
	v_mov_b32_e32 v97, v2
	v_mov_b32_e32 v108, v2
	v_mov_b32_e32 v109, v2
	v_mov_b32_e32 v110, v2
	v_mov_b32_e32 v111, v2
	v_mov_b32_e32 v112, v2
	v_mov_b32_e32 v113, v2
	v_mov_b32_e32 v114, v2
	v_mov_b32_e32 v115, v2
	v_mov_b32_e32 v124, v2
	v_mov_b32_e32 v125, v2
	v_mov_b32_e32 v126, v2
	v_mov_b32_e32 v127, v2
	v_mov_b32_e32 v128, v2
	v_mov_b32_e32 v129, v2
	v_mov_b32_e32 v130, v2
	v_mov_b32_e32 v131, v2
	.p2alignl 6, 3212836864

.LBB0_1400:
	s_add_u32 s76, s38, 0x100
	s_addc_u32 s78, s39, 0
	s_add_u32 s6, s14, 0x42080
	s_addc_u32 s7, s15, 0
	v_mov_b32_e32 v2, 0
	v_lshl_add_u64 v[142:143], s[6:7], 0, v[138:139]
	v_lshl_add_u64 v[144:145], s[6:7], 0, v[140:141]
	s_mov_b32 s79, -2
	s_mov_b64 s[36:37], 0
	v_mov_b32_e32 v3, v2
	v_mov_b32_e32 v4, v2
	v_mov_b32_e32 v5, v2
	v_mov_b32_e32 v6, v2
	v_mov_b32_e32 v7, v2
	v_mov_b32_e32 v8, v2
	v_mov_b32_e32 v9, v2
	v_mov_b32_e32 v10, v2
	v_mov_b32_e32 v11, v2
	v_mov_b32_e32 v12, v2
	v_mov_b32_e32 v13, v2
	v_mov_b32_e32 v14, v2
	v_mov_b32_e32 v15, v2
	v_mov_b32_e32 v16, v2
	v_mov_b32_e32 v17, v2
	v_mov_b32_e32 v18, v2
	v_mov_b32_e32 v19, v2
	v_mov_b32_e32 v20, v2
	v_mov_b32_e32 v21, v2
	v_mov_b32_e32 v22, v2
	v_mov_b32_e32 v23, v2
	v_mov_b32_e32 v24, v2
	v_mov_b32_e32 v25, v2
	v_mov_b32_e32 v26, v2
	v_mov_b32_e32 v27, v2
	v_mov_b32_e32 v28, v2
	v_mov_b32_e32 v29, v2
	v_mov_b32_e32 v30, v2
	v_mov_b32_e32 v31, v2
	v_mov_b32_e32 v32, v2
	v_mov_b32_e32 v33, v2
	v_mov_b32_e32 v50, v2
	v_mov_b32_e32 v51, v2
	v_mov_b32_e32 v52, v2
	v_mov_b32_e32 v53, v2
	v_mov_b32_e32 v54, v2
	v_mov_b32_e32 v55, v2
	v_mov_b32_e32 v56, v2
	v_mov_b32_e32 v57, v2
	v_mov_b32_e32 v66, v2
	v_mov_b32_e32 v67, v2
	v_mov_b32_e32 v68, v2
	v_mov_b32_e32 v69, v2
	v_mov_b32_e32 v70, v2
	v_mov_b32_e32 v71, v2
	v_mov_b32_e32 v72, v2
	v_mov_b32_e32 v73, v2
	v_mov_b32_e32 v78, v2
	v_mov_b32_e32 v79, v2
	v_mov_b32_e32 v80, v2
	v_mov_b32_e32 v81, v2
	v_mov_b32_e32 v86, v2
	v_mov_b32_e32 v87, v2
	v_mov_b32_e32 v88, v2
	v_mov_b32_e32 v89, v2
	v_mov_b32_e32 v90, v2
	v_mov_b32_e32 v91, v2
	v_mov_b32_e32 v92, v2
	v_mov_b32_e32 v93, v2
	v_mov_b32_e32 v94, v2
	v_mov_b32_e32 v95, v2
	v_mov_b32_e32 v96, v2
	v_mov_b32_e32 v97, v2
	v_mov_b32_e32 v34, v2
	v_mov_b32_e32 v35, v2
	v_mov_b32_e32 v36, v2
	v_mov_b32_e32 v37, v2
	v_mov_b32_e32 v38, v2
	v_mov_b32_e32 v39, v2
	v_mov_b32_e32 v40, v2
	v_mov_b32_e32 v41, v2
	v_mov_b32_e32 v42, v2
	v_mov_b32_e32 v43, v2
	v_mov_b32_e32 v44, v2
	v_mov_b32_e32 v45, v2
	v_mov_b32_e32 v46, v2
	v_mov_b32_e32 v47, v2
	v_mov_b32_e32 v48, v2
	v_mov_b32_e32 v49, v2
	v_mov_b32_e32 v58, v2
	v_mov_b32_e32 v59, v2
	v_mov_b32_e32 v60, v2
	v_mov_b32_e32 v61, v2
	v_mov_b32_e32 v62, v2
	v_mov_b32_e32 v63, v2
	v_mov_b32_e32 v64, v2
	v_mov_b32_e32 v65, v2
	v_mov_b32_e32 v74, v2
	v_mov_b32_e32 v75, v2
	v_mov_b32_e32 v76, v2
	v_mov_b32_e32 v77, v2
	v_mov_b32_e32 v82, v2
	v_mov_b32_e32 v83, v2
	v_mov_b32_e32 v84, v2
	v_mov_b32_e32 v85, v2
	v_mov_b32_e32 v100, v2
	v_mov_b32_e32 v101, v2
	v_mov_b32_e32 v102, v2
	v_mov_b32_e32 v103, v2
	v_mov_b32_e32 v104, v2
	v_mov_b32_e32 v105, v2
	v_mov_b32_e32 v106, v2
	v_mov_b32_e32 v107, v2
	v_mov_b32_e32 v108, v2
	v_mov_b32_e32 v109, v2
	v_mov_b32_e32 v110, v2
	v_mov_b32_e32 v111, v2
	v_mov_b32_e32 v112, v2
	v_mov_b32_e32 v113, v2
	v_mov_b32_e32 v114, v2
	v_mov_b32_e32 v115, v2
	v_mov_b32_e32 v116, v2
	v_mov_b32_e32 v117, v2
	v_mov_b32_e32 v118, v2
	v_mov_b32_e32 v119, v2
	v_mov_b32_e32 v120, v2
	v_mov_b32_e32 v121, v2
	v_mov_b32_e32 v122, v2
	v_mov_b32_e32 v123, v2
	v_mov_b32_e32 v124, v2
	v_mov_b32_e32 v125, v2
	v_mov_b32_e32 v126, v2
	v_mov_b32_e32 v127, v2
	v_mov_b32_e32 v128, v2
	v_mov_b32_e32 v129, v2
	v_mov_b32_e32 v130, v2
	v_mov_b32_e32 v131, v2
	.p2alignl 6, 3212836864

.LBB0_1420:
	s_ashr_i32 s43, s42, 31
	s_lshl_b64 s[6:7], s[42:43], 17
	s_add_u32 s46, s81, s6
	s_addc_u32 s47, s82, s7
	s_and_b64 s[6:7], s[36:37], exec
	v_mov_b32_e32 v2, 0
	s_cselect_b32 s43, s47, s3
	s_cselect_b32 s79, s46, s2
	s_mov_b32 s50, 0
	s_mov_b64 s[36:37], -1
	s_mov_b64 s[48:49], 0
	v_mov_b32_e32 v3, v2
	v_mov_b32_e32 v4, v2
	v_mov_b32_e32 v5, v2
	v_mov_b32_e32 v6, v2
	v_mov_b32_e32 v7, v2
	v_mov_b32_e32 v8, v2
	v_mov_b32_e32 v9, v2
	v_mov_b32_e32 v18, v2
	v_mov_b32_e32 v19, v2
	v_mov_b32_e32 v20, v2
	v_mov_b32_e32 v21, v2
	v_mov_b32_e32 v22, v2
	v_mov_b32_e32 v23, v2
	v_mov_b32_e32 v24, v2
	v_mov_b32_e32 v25, v2
	v_mov_b32_e32 v34, v2
	v_mov_b32_e32 v35, v2
	v_mov_b32_e32 v36, v2
	v_mov_b32_e32 v37, v2
	v_mov_b32_e32 v38, v2
	v_mov_b32_e32 v39, v2
	v_mov_b32_e32 v40, v2
	v_mov_b32_e32 v41, v2
	v_mov_b32_e32 v50, v2
	v_mov_b32_e32 v51, v2
	v_mov_b32_e32 v52, v2
	v_mov_b32_e32 v53, v2
	v_mov_b32_e32 v54, v2
	v_mov_b32_e32 v55, v2
	v_mov_b32_e32 v56, v2
	v_mov_b32_e32 v57, v2
	v_mov_b32_e32 v10, v2
	v_mov_b32_e32 v11, v2
	v_mov_b32_e32 v12, v2
	v_mov_b32_e32 v13, v2
	v_mov_b32_e32 v14, v2
	v_mov_b32_e32 v15, v2
	v_mov_b32_e32 v16, v2
	v_mov_b32_e32 v17, v2
	v_mov_b32_e32 v26, v2
	v_mov_b32_e32 v27, v2
	v_mov_b32_e32 v28, v2
	v_mov_b32_e32 v29, v2
	v_mov_b32_e32 v30, v2
	v_mov_b32_e32 v31, v2
	v_mov_b32_e32 v32, v2
	v_mov_b32_e32 v33, v2
	v_mov_b32_e32 v42, v2
	v_mov_b32_e32 v43, v2
	v_mov_b32_e32 v44, v2
	v_mov_b32_e32 v45, v2
	v_mov_b32_e32 v46, v2
	v_mov_b32_e32 v47, v2
	v_mov_b32_e32 v48, v2
	v_mov_b32_e32 v49, v2
	v_mov_b32_e32 v58, v2
	v_mov_b32_e32 v59, v2
	v_mov_b32_e32 v60, v2
	v_mov_b32_e32 v61, v2
	v_mov_b32_e32 v62, v2
	v_mov_b32_e32 v63, v2
	v_mov_b32_e32 v64, v2
	v_mov_b32_e32 v65, v2
	v_mov_b32_e32 v66, v2
	v_mov_b32_e32 v67, v2
	v_mov_b32_e32 v68, v2
	v_mov_b32_e32 v69, v2
	v_mov_b32_e32 v70, v2
	v_mov_b32_e32 v71, v2
	v_mov_b32_e32 v72, v2
	v_mov_b32_e32 v73, v2
	v_mov_b32_e32 v82, v2
	v_mov_b32_e32 v83, v2
	v_mov_b32_e32 v84, v2
	v_mov_b32_e32 v85, v2
	v_mov_b32_e32 v90, v2
	v_mov_b32_e32 v91, v2
	v_mov_b32_e32 v92, v2
	v_mov_b32_e32 v93, v2
	v_mov_b32_e32 v116, v2
	v_mov_b32_e32 v117, v2
	v_mov_b32_e32 v118, v2
	v_mov_b32_e32 v119, v2
	v_mov_b32_e32 v120, v2
	v_mov_b32_e32 v121, v2
	v_mov_b32_e32 v122, v2
	v_mov_b32_e32 v123, v2
	v_mov_b32_e32 v140, v2
	v_mov_b32_e32 v141, v2
	v_mov_b32_e32 v142, v2
	v_mov_b32_e32 v143, v2
	v_mov_b32_e32 v144, v2
	v_mov_b32_e32 v145, v2
	v_mov_b32_e32 v146, v2
	v_mov_b32_e32 v147, v2
	v_mov_b32_e32 v74, v2
	v_mov_b32_e32 v75, v2
	v_mov_b32_e32 v76, v2
	v_mov_b32_e32 v77, v2
	v_mov_b32_e32 v78, v2
	v_mov_b32_e32 v79, v2
	v_mov_b32_e32 v80, v2
	v_mov_b32_e32 v81, v2
	v_mov_b32_e32 v108, v2
	v_mov_b32_e32 v109, v2
	v_mov_b32_e32 v110, v2
	v_mov_b32_e32 v111, v2
	v_mov_b32_e32 v112, v2
	v_mov_b32_e32 v113, v2
	v_mov_b32_e32 v114, v2
	v_mov_b32_e32 v115, v2
	v_mov_b32_e32 v128, v2
	v_mov_b32_e32 v129, v2
	v_mov_b32_e32 v130, v2
	v_mov_b32_e32 v131, v2
	v_mov_b32_e32 v132, v2
	v_mov_b32_e32 v133, v2
	v_mov_b32_e32 v134, v2
	v_mov_b32_e32 v135, v2
	v_mov_b32_e32 v148, v2
	v_mov_b32_e32 v149, v2
	v_mov_b32_e32 v150, v2
	v_mov_b32_e32 v151, v2
	v_mov_b32_e32 v152, v2
	v_mov_b32_e32 v153, v2
	v_mov_b32_e32 v154, v2
	v_mov_b32_e32 v155, v2
	.p2alignl 6, 3212836864

.LBB0_1579:
	v_lshlrev_b32_e32 v36, 5, v179
	v_and_b32_e32 v36, 0x180, v36
	v_lshlrev_b32_e32 v38, 3, v179
	v_lshl_or_b32 v36, v98, 9, v36
	v_lshlrev_b32_e32 v37, 5, v187
	v_and_b32_e32 v38, 24, v38
	v_or3_b32 v36, v36, v37, v38
	v_lshlrev_b32_e32 v37, 6, v186
	v_and_or_b32 v209, v37, 64, v36
	v_bitop3_b32 v210, v36, 64, v37 bitop3:0x34
	v_and_b32_e32 v37, 7, v179
	v_and_b32_e32 v36, 30, v188
	v_lshlrev_b32_e32 v229, 10, v37
	v_lshlrev_b32_e32 v37, 4, v37
	v_lshl_or_b32 v200, v36, 11, v37
	v_lshrrev_b32_e32 v36, 1, v179
	v_and_b32_e32 v228, 28, v36
	v_lshlrev_b32_e32 v36, 3, v185
	v_and_b32_e32 v37, 4, v179
	v_and_or_b32 v36, v36, 24, v37
	v_lshlrev_b32_e32 v198, 2, v36
	v_bitop3_b32 v36, v179, 5, 7 bitop3:0x6c
	v_bfe_u32 v39, v188, 2, 3
	v_lshlrev_b32_e32 v37, 3, v36
	v_bitop3_b32 v39, v39, v179, 7 bitop3:0x78
	v_bitop3_b32 v36, v37, 28, v36 bitop3:0xc8
	v_lshlrev_b32_e32 v230, 4, v39
	v_lshlrev_b32_e32 v39, 2, v188
	v_lshlrev_b32_e32 v188, 2, v36
	v_bitop3_b32 v36, v179, 6, 7 bitop3:0x6c
	v_lshlrev_b32_e32 v37, 3, v36
	v_bitop3_b32 v36, v37, 28, v36 bitop3:0xc8
	s_lshl_b32 s4, s76, 10
	v_lshlrev_b32_e32 v186, 2, v36
	v_bitop3_b32 v36, v179, 7, v179 bitop3:0xc
	s_waitcnt lgkmcnt(0)
	s_barrier
	s_sub_i32 s17, 0, s4
	v_lshlrev_b32_e32 v37, 3, v36
	s_add_i32 s4, 0, 0x8000
	s_lshl_b32 s15, s76, 4
	v_mov_b32_e32 v177, v99
	v_add_u32_e32 v38, 0, v229
	v_and_b32_e32 v231, 8, v39
	v_bitop3_b32 v36, v37, 28, v36 bitop3:0xc8
	v_add_u32_e32 v205, s4, v209
	v_add_u32_e32 v67, s4, v210
	s_add_i32 s4, 0, 0x6000
	v_lshlrev_b32_e32 v35, 3, v175
	s_lshl_b32 s12, s40, 6
	s_mov_b32 s14, 3
	s_add_i32 s16, s41, 0
	v_lshl_add_u64 v[202:203], s[56:57], 0, v[176:177]
	v_and_b32_e32 v232, -2, v189
	v_add3_u32 v233, v38, v230, v231
	v_mov_b32_e32 v201, v99
	s_lshl_b32 s13, s78, 1
	v_mov_b32_e32 v199, v99
	v_xor_b32_e32 v196, 32, v198
	v_mov_b32_e32 v197, v99
	v_xor_b32_e32 v194, 64, v198
	v_mov_b32_e32 v195, v99
	v_xor_b32_e32 v192, 0x60, v198
	v_mov_b32_e32 v193, v99
	v_xor_b32_e32 v190, 16, v198
	v_mov_b32_e32 v191, v99
	v_mov_b32_e32 v189, v99
	v_mov_b32_e32 v187, v99
	v_lshlrev_b32_e32 v64, 2, v36
	v_mov_b32_e32 v65, v99
	v_cmp_eq_u32_e64 s[34:35], 0, v185
	v_mov_b32_e32 v175, v99
	v_mov_b32_e32 v179, v99
	v_mov_b32_e32 v185, v99
	v_add_u32_e32 v234, s4, v209
	v_add_u32_e32 v235, s4, v210
	s_add_i32 s18, s15, 0x80
	.p2alignl 6, 3212836864

.LBB0_1759:
	v_bfe_u32 v178, v16, 4, 2
	v_and_b32_e32 v17, 15, v16
	v_lshlrev_b32_e32 v18, 4, v178
	v_lshlrev_b32_e32 v16, 2, v16
	s_and_b32 s26, s17, 3
	v_lshl_or_b32 v138, s18, 6, v17
	v_lshl_or_b32 v17, v17, 6, v18
	s_lshl_b32 s17, s18, 13
	v_and_b32_e32 v16, 32, v16
	s_add_i32 m0, s31, 0x18000
	v_lshl_add_u64 v[8:9], v[8:9], 0, s[0:1]
	v_bitop3_b32 v18, v17, s17, v16 bitop3:0xde
	s_lshl_b32 s17, s26, 12
	s_waitcnt vmcnt(2)
	s_barrier
	global_load_lds_dwordx4 v[8:9], off
	v_lshl_add_u64 v[6:7], v[6:7], 0, s[0:1]
	s_add_i32 m0, s31, 0x1a000
	s_add_i32 s39, s31, 0x8000
	s_add_i32 s40, s31, 0xa000
	global_load_lds_dwordx4 v[6:7], off
	v_lshl_add_u64 v[4:5], v[4:5], 0, s[0:1]
	s_mov_b32 m0, s39
	s_add_u32 s18, s2, 0x40080
	global_load_lds_dwordx4 v[4:5], off
	v_lshl_add_u64 v[2:3], v[2:3], 0, s[0:1]
	s_mov_b32 m0, s40
	s_addc_u32 s19, s3, 0
	global_load_lds_dwordx4 v[2:3], off
	s_add_i32 m0, s31, 0x1c000
	v_lshl_add_u64 v[2:3], s[18:19], 0, v[98:99]
	global_load_lds_dwordx4 v[2:3], off
	v_lshl_add_u64 v[2:3], s[18:19], 0, v[132:133]
	s_add_i32 m0, s31, 0x1e000
	v_bitop3_b32 v139, v17, s17, v16 bitop3:0xde
	global_load_lds_dwordx4 v[2:3], off
	s_waitcnt vmcnt(6)
	s_barrier
	v_readlane_b32 s17, v255, 13
	v_readlane_b32 s18, v255, 11
	s_add_u32 s17, s17, s16
	v_readlane_b32 s19, v255, 12
	s_addc_u32 s18, s19, 0
	v_readlane_b32 s19, v254, 10
	v_lshlrev_b32_e32 v2, 14, v10
	s_add_u32 s41, s19, s17
	v_readlane_b32 s17, v254, 11
	v_and_b32_e32 v2, 0xffff8000, v2
	s_addc_u32 s42, s17, s18
	v_lshl_add_u32 v2, v12, 11, v2
	v_and_b32_e32 v3, 1, v10
	v_readlane_b32 s17, v254, 13
	v_lshl_or_b32 v2, v3, 6, v2
	s_add_u32 s16, s17, s16
	v_readlane_b32 s17, v254, 14
	v_lshl_add_u32 v2, v13, 1, v2
	v_mov_b32_e32 v3, v99
	s_addc_u32 s17, s17, 0
	v_lshl_add_u64 v[134:135], s[16:17], 0, v[2:3]
	v_lshlrev_b32_e32 v2, 14, v11
	v_and_b32_e32 v2, 0xffff8000, v2
	v_lshl_add_u32 v2, v14, 11, v2
	v_and_b32_e32 v3, 1, v11
	v_lshl_or_b32 v2, v3, 6, v2
	v_lshl_add_u32 v2, v15, 1, v2
	v_mov_b32_e32 v3, v99
	v_lshl_add_u64 v[136:137], s[16:17], 0, v[2:3]
	v_mov_b32_e32 v2, 0
	s_mov_b32 s43, -2
	s_mov_b64 s[16:17], 0
	v_add_u32_e32 v140, 0, v18
	v_mov_b32_e32 v3, v2
	v_mov_b32_e32 v4, v2
	v_mov_b32_e32 v5, v2
	v_mov_b32_e32 v6, v2
	v_mov_b32_e32 v7, v2
	v_mov_b32_e32 v8, v2
	v_mov_b32_e32 v9, v2
	v_mov_b32_e32 v10, v2
	v_mov_b32_e32 v11, v2
	v_mov_b32_e32 v12, v2
	v_mov_b32_e32 v13, v2
	v_mov_b32_e32 v14, v2
	v_mov_b32_e32 v15, v2
	v_mov_b32_e32 v16, v2
	v_mov_b32_e32 v17, v2
	v_mov_b32_e32 v18, v2
	v_mov_b32_e32 v19, v2
	v_mov_b32_e32 v20, v2
	v_mov_b32_e32 v21, v2
	v_mov_b32_e32 v22, v2
	v_mov_b32_e32 v23, v2
	v_mov_b32_e32 v24, v2
	v_mov_b32_e32 v25, v2
	v_mov_b32_e32 v26, v2
	v_mov_b32_e32 v27, v2
	v_mov_b32_e32 v28, v2
	v_mov_b32_e32 v29, v2
	v_mov_b32_e32 v30, v2
	v_mov_b32_e32 v31, v2
	v_mov_b32_e32 v32, v2
	v_mov_b32_e32 v33, v2
	v_mov_b32_e32 v66, v2
	v_mov_b32_e32 v67, v2
	v_mov_b32_e32 v68, v2
	v_mov_b32_e32 v69, v2
	v_mov_b32_e32 v70, v2
	v_mov_b32_e32 v71, v2
	v_mov_b32_e32 v72, v2
	v_mov_b32_e32 v73, v2
	v_mov_b32_e32 v74, v2
	v_mov_b32_e32 v75, v2
	v_mov_b32_e32 v76, v2
	v_mov_b32_e32 v77, v2
	v_mov_b32_e32 v78, v2
	v_mov_b32_e32 v79, v2
	v_mov_b32_e32 v80, v2
	v_mov_b32_e32 v81, v2
	v_mov_b32_e32 v82, v2
	v_mov_b32_e32 v83, v2
	v_mov_b32_e32 v84, v2
	v_mov_b32_e32 v85, v2
	v_mov_b32_e32 v86, v2
	v_mov_b32_e32 v87, v2
	v_mov_b32_e32 v88, v2
	v_mov_b32_e32 v89, v2
	v_mov_b32_e32 v90, v2
	v_mov_b32_e32 v91, v2
	v_mov_b32_e32 v92, v2
	v_mov_b32_e32 v93, v2
	v_mov_b32_e32 v94, v2
	v_mov_b32_e32 v95, v2
	v_mov_b32_e32 v96, v2
	v_mov_b32_e32 v97, v2
	v_mov_b32_e32 v34, v2
	v_mov_b32_e32 v35, v2
	v_mov_b32_e32 v36, v2
	v_mov_b32_e32 v37, v2
	v_mov_b32_e32 v38, v2
	v_mov_b32_e32 v39, v2
	v_mov_b32_e32 v40, v2
	v_mov_b32_e32 v41, v2
	v_mov_b32_e32 v42, v2
	v_mov_b32_e32 v43, v2
	v_mov_b32_e32 v44, v2
	v_mov_b32_e32 v45, v2
	v_mov_b32_e32 v46, v2
	v_mov_b32_e32 v47, v2
	v_mov_b32_e32 v48, v2
	v_mov_b32_e32 v49, v2
	v_mov_b32_e32 v50, v2
	v_mov_b32_e32 v51, v2
	v_mov_b32_e32 v52, v2
	v_mov_b32_e32 v53, v2
	v_mov_b32_e32 v54, v2
	v_mov_b32_e32 v55, v2
	v_mov_b32_e32 v56, v2
	v_mov_b32_e32 v57, v2
	v_mov_b32_e32 v58, v2
	v_mov_b32_e32 v59, v2
	v_mov_b32_e32 v60, v2
	v_mov_b32_e32 v61, v2
	v_mov_b32_e32 v62, v2
	v_mov_b32_e32 v63, v2
	v_mov_b32_e32 v64, v2
	v_mov_b32_e32 v65, v2
	v_mov_b32_e32 v100, v2
	v_mov_b32_e32 v101, v2
	v_mov_b32_e32 v102, v2
	v_mov_b32_e32 v103, v2
	v_mov_b32_e32 v104, v2
	v_mov_b32_e32 v105, v2
	v_mov_b32_e32 v106, v2
	v_mov_b32_e32 v107, v2
	v_mov_b32_e32 v108, v2
	v_mov_b32_e32 v109, v2
	v_mov_b32_e32 v110, v2
	v_mov_b32_e32 v111, v2
	v_mov_b32_e32 v112, v2
	v_mov_b32_e32 v113, v2
	v_mov_b32_e32 v114, v2
	v_mov_b32_e32 v115, v2
	v_mov_b32_e32 v116, v2
	v_mov_b32_e32 v117, v2
	v_mov_b32_e32 v118, v2
	v_mov_b32_e32 v119, v2
	v_mov_b32_e32 v120, v2
	v_mov_b32_e32 v121, v2
	v_mov_b32_e32 v122, v2
	v_mov_b32_e32 v123, v2
	v_mov_b32_e32 v124, v2
	v_mov_b32_e32 v125, v2
	v_mov_b32_e32 v126, v2
	v_mov_b32_e32 v127, v2
	v_mov_b32_e32 v128, v2
	v_mov_b32_e32 v129, v2
	v_mov_b32_e32 v130, v2
	v_mov_b32_e32 v131, v2
	.p2alignl 6, 3212836864

.LBB0_1846:
	s_ashr_i32 s19, s18, 31
	s_lshl_b64 s[36:37], s[18:19], 19
	s_add_u32 s36, s24, s36
	s_addc_u32 s37, s25, s37
	s_ashr_i32 s17, s16, 31
	s_lshl_b64 s[38:39], s[16:17], 19
	s_add_u32 s38, s26, s38
	s_addc_u32 s39, s27, s39
	s_and_b64 s[44:45], s[34:35], exec
	s_cselect_b32 s17, s39, s43
	s_cselect_b32 s19, s38, s42
	s_add_u32 s31, s42, 0x100
	s_addc_u32 s76, s43, 0
	s_add_u32 s42, s40, 0x40080
	s_addc_u32 s43, s41, 0
	v_mov_b32_e32 v2, 0
	v_lshl_add_u64 v[116:117], s[42:43], 0, v[176:177]
	v_lshl_add_u64 v[118:119], s[42:43], 0, v[178:179]
	s_mov_b32 s78, -2
	s_mov_b64 s[42:43], 0
	v_mov_b32_e32 v3, v2
	v_mov_b32_e32 v4, v2
	v_mov_b32_e32 v5, v2
	v_mov_b32_e32 v6, v2
	v_mov_b32_e32 v7, v2
	v_mov_b32_e32 v8, v2
	v_mov_b32_e32 v9, v2
	v_mov_b32_e32 v18, v2
	v_mov_b32_e32 v19, v2
	v_mov_b32_e32 v20, v2
	v_mov_b32_e32 v21, v2
	v_mov_b32_e32 v22, v2
	v_mov_b32_e32 v23, v2
	v_mov_b32_e32 v24, v2
	v_mov_b32_e32 v25, v2
	s_waitcnt vmcnt(0)
	v_mov_b32_e32 v34, v2
	v_mov_b32_e32 v35, v2
	v_mov_b32_e32 v36, v2
	v_mov_b32_e32 v37, v2
	v_mov_b32_e32 v38, v2
	v_mov_b32_e32 v39, v2
	v_mov_b32_e32 v40, v2
	v_mov_b32_e32 v41, v2
	v_mov_b32_e32 v50, v2
	v_mov_b32_e32 v51, v2
	v_mov_b32_e32 v52, v2
	v_mov_b32_e32 v53, v2
	v_mov_b32_e32 v54, v2
	v_mov_b32_e32 v55, v2
	v_mov_b32_e32 v56, v2
	v_mov_b32_e32 v57, v2
	v_mov_b32_e32 v10, v2
	v_mov_b32_e32 v11, v2
	v_mov_b32_e32 v12, v2
	v_mov_b32_e32 v13, v2
	v_mov_b32_e32 v14, v2
	v_mov_b32_e32 v15, v2
	v_mov_b32_e32 v16, v2
	v_mov_b32_e32 v17, v2
	v_mov_b32_e32 v26, v2
	v_mov_b32_e32 v27, v2
	v_mov_b32_e32 v28, v2
	v_mov_b32_e32 v29, v2
	v_mov_b32_e32 v30, v2
	v_mov_b32_e32 v31, v2
	v_mov_b32_e32 v32, v2
	v_mov_b32_e32 v33, v2
	v_mov_b32_e32 v42, v2
	v_mov_b32_e32 v43, v2
	v_mov_b32_e32 v44, v2
	v_mov_b32_e32 v45, v2
	v_mov_b32_e32 v46, v2
	v_mov_b32_e32 v47, v2
	v_mov_b32_e32 v48, v2
	v_mov_b32_e32 v49, v2
	v_mov_b32_e32 v58, v2
	v_mov_b32_e32 v59, v2
	v_mov_b32_e32 v60, v2
	v_mov_b32_e32 v61, v2
	v_mov_b32_e32 v62, v2
	v_mov_b32_e32 v63, v2
	v_mov_b32_e32 v64, v2
	v_mov_b32_e32 v65, v2
	v_mov_b32_e32 v66, v2
	v_mov_b32_e32 v67, v2
	v_mov_b32_e32 v68, v2
	v_mov_b32_e32 v69, v2
	v_mov_b32_e32 v70, v2
	v_mov_b32_e32 v71, v2
	v_mov_b32_e32 v72, v2
	v_mov_b32_e32 v73, v2
	v_mov_b32_e32 v82, v2
	v_mov_b32_e32 v83, v2
	v_mov_b32_e32 v84, v2
	v_mov_b32_e32 v85, v2
	v_mov_b32_e32 v86, v2
	v_mov_b32_e32 v87, v2
	v_mov_b32_e32 v88, v2
	v_mov_b32_e32 v89, v2
	v_mov_b32_e32 v100, v2
	v_mov_b32_e32 v101, v2
	v_mov_b32_e32 v102, v2
	v_mov_b32_e32 v103, v2
	v_mov_b32_e32 v104, v2
	v_mov_b32_e32 v105, v2
	v_mov_b32_e32 v106, v2
	v_mov_b32_e32 v107, v2
	v_mov_b32_e32 v132, v2
	v_mov_b32_e32 v133, v2
	v_mov_b32_e32 v134, v2
	v_mov_b32_e32 v135, v2
	v_mov_b32_e32 v136, v2
	v_mov_b32_e32 v137, v2
	v_mov_b32_e32 v138, v2
	v_mov_b32_e32 v139, v2
	v_mov_b32_e32 v74, v2
	v_mov_b32_e32 v75, v2
	v_mov_b32_e32 v76, v2
	v_mov_b32_e32 v77, v2
	v_mov_b32_e32 v78, v2
	v_mov_b32_e32 v79, v2
	v_mov_b32_e32 v80, v2
	v_mov_b32_e32 v81, v2
	v_mov_b32_e32 v90, v2
	v_mov_b32_e32 v91, v2
	v_mov_b32_e32 v92, v2
	v_mov_b32_e32 v93, v2
	v_mov_b32_e32 v94, v2
	v_mov_b32_e32 v95, v2
	v_mov_b32_e32 v96, v2
	v_mov_b32_e32 v97, v2
	v_mov_b32_e32 v108, v2
	v_mov_b32_e32 v109, v2
	v_mov_b32_e32 v110, v2
	v_mov_b32_e32 v111, v2
	v_mov_b32_e32 v112, v2
	v_mov_b32_e32 v113, v2
	v_mov_b32_e32 v114, v2
	v_mov_b32_e32 v115, v2
	v_mov_b32_e32 v140, v2
	v_mov_b32_e32 v141, v2
	v_mov_b32_e32 v142, v2
	v_mov_b32_e32 v143, v2
	v_mov_b32_e32 v144, v2
	v_mov_b32_e32 v145, v2
	v_mov_b32_e32 v146, v2
	v_mov_b32_e32 v147, v2
	.p2alignl 6, 3212836864

.LBB0_1983:
	v_and_or_b32 v89, v189, 3, v187
	v_lshlrev_b32_e32 v89, 7, v89
	v_lshlrev_b32_e32 v87, 5, v87
	v_and_b32_e32 v88, 24, v88
	s_waitcnt lgkmcnt(0)
	s_barrier
	v_or3_b32 v87, v89, v87, v88
	v_lshlrev_b32_e32 v86, 6, v86
	v_and_or_b32 v177, v86, 64, v87
	v_bitop3_b32 v178, v87, 64, v86 bitop3:0x34
	s_cmp_lt_i32 s85, 3
	s_cbranch_scc1 .LBB0_2059
	v_mov_b32_e32 v149, v99
	v_ashrrev_i32_e32 v86, 6, v185
	v_and_b32_e32 v87, 7, v185
	v_lshl_add_u64 v[154:155], s[18:19], 0, v[148:149]
	v_and_b32_e32 v149, -2, v86
	v_and_b32_e32 v86, 30, v189
	v_lshl_add_u32 v88, v87, 10, 0
	v_lshlrev_b32_e32 v87, 4, v87
	v_lshl_or_b32 v156, v86, 11, v87
	v_lshlrev_b32_e32 v86, 3, v179
	v_and_b32_e32 v87, 4, v185
	v_and_or_b32 v86, v86, 24, v87
	v_lshlrev_b32_e32 v158, 2, v86
	v_bitop3_b32 v86, v185, 5, 7 bitop3:0x6c
	v_lshlrev_b32_e32 v87, 3, v86
	v_bitop3_b32 v86, v87, 28, v86 bitop3:0xc8
	v_lshlrev_b32_e32 v168, 2, v86
	v_bitop3_b32 v86, v185, 6, 7 bitop3:0x6c
	v_lshlrev_b32_e32 v87, 3, v86
	v_bitop3_b32 v86, v87, 28, v86 bitop3:0xc8
	v_lshlrev_b32_e32 v170, 2, v86
	v_bitop3_b32 v86, v185, 7, v185 bitop3:0xc
	v_bfe_u32 v89, v189, 2, 3
	v_lshlrev_b32_e32 v87, 3, v86
	s_add_i32 s4, 0, 0x4000
	v_bitop3_b32 v89, v89, v185, 7 bitop3:0x78
	v_lshlrev_b32_e32 v90, 2, v189
	v_bitop3_b32 v86, v87, 28, v86 bitop3:0xc8
	v_add_u32_e32 v200, s4, v177
	v_add_u32_e32 v201, s4, v178
	s_add_i32 s4, 0, 0x6000
	v_lshlrev_b32_e32 v89, 4, v89
	v_and_b32_e32 v90, 8, v90
	v_lshlrev_b32_e32 v172, 2, v86
	v_add_u32_e32 v202, s4, v177
	v_add_u32_e32 v203, s4, v178
	v_add_u32_e32 v86, s86, v187
	s_sub_i32 s4, s89, s86
	s_lshl_b32 s97, s90, 4
	s_lshl_b32 s2, s90, 11
	v_add3_u32 v198, v88, v89, v90
	v_mov_b32_e32 v157, v99
	s_lshl_b32 s3, s91, 1
	v_and_b32_e32 v199, 28, v186
	s_mov_b32 s76, 3
	v_mov_b32_e32 v159, v99
	v_xor_b32_e32 v160, 32, v158
	v_mov_b32_e32 v161, v99
	v_xor_b32_e32 v162, 64, v158
	v_mov_b32_e32 v163, v99
	v_xor_b32_e32 v164, 0x60, v158
	v_mov_b32_e32 v165, v99
	v_xor_b32_e32 v166, 16, v158
	v_mov_b32_e32 v167, v99
	v_mov_b32_e32 v169, v99
	v_mov_b32_e32 v171, v99
	v_mov_b32_e32 v173, v99
	s_mov_b32 s14, 0
	v_cmp_eq_u32_e64 s[36:37], 0, v179
	v_mov_b32_e32 v151, v99
	v_mov_b32_e32 v153, v99
	s_sub_i32 s56, s86, s89
	v_sub_u32_e32 v204, v86, v176
	s_add_i32 s6, s4, 0xffffff9f
	.p2alignl 6, 3212836864

.LBB0_2259:
	v_bfe_u32 v194, v16, 4, 2
	v_and_b32_e32 v17, 15, v16
	v_lshlrev_b32_e32 v18, 4, v194
	v_lshlrev_b32_e32 v16, 2, v16
	s_and_b32 s24, s19, 3
	v_lshl_or_b32 v138, s22, 6, v17
	v_lshl_or_b32 v17, v17, 6, v18
	s_lshl_b32 s19, s22, 13
	v_and_b32_e32 v16, 32, v16
	s_add_i32 m0, s26, 0x18000
	v_lshl_add_u64 v[8:9], v[8:9], 0, s[0:1]
	v_bitop3_b32 v18, v17, s19, v16 bitop3:0xde
	s_lshl_b32 s19, s24, 12
	s_waitcnt vmcnt(2)
	s_barrier
	global_load_lds_dwordx4 v[8:9], off
	v_lshl_add_u64 v[6:7], v[6:7], 0, s[0:1]
	s_add_i32 m0, s26, 0x1a000
	s_add_i32 s39, s26, 0x8000
	s_add_i32 s40, s26, 0xa000
	global_load_lds_dwordx4 v[6:7], off
	v_lshl_add_u64 v[4:5], v[4:5], 0, s[0:1]
	s_mov_b32 m0, s39
	s_add_u32 s34, s2, 0x40080
	global_load_lds_dwordx4 v[4:5], off
	v_lshl_add_u64 v[2:3], v[2:3], 0, s[0:1]
	s_mov_b32 m0, s40
	s_addc_u32 s35, s3, 0
	global_load_lds_dwordx4 v[2:3], off
	s_add_i32 m0, s26, 0x1c000
	v_lshl_add_u64 v[2:3], s[34:35], 0, v[98:99]
	global_load_lds_dwordx4 v[2:3], off
	v_lshl_add_u64 v[2:3], s[34:35], 0, v[132:133]
	s_add_i32 m0, s26, 0x1e000
	v_bitop3_b32 v139, v17, s19, v16 bitop3:0xde
	global_load_lds_dwordx4 v[2:3], off
	s_waitcnt vmcnt(6)
	s_barrier
	v_readlane_b32 s19, v255, 13
	v_readlane_b32 s34, v255, 11
	s_add_u32 s19, s19, s18
	v_readlane_b32 s35, v255, 12
	s_addc_u32 s22, s35, 0
	v_readlane_b32 s28, v254, 24
	v_lshlrev_b32_e32 v2, 14, v10
	s_add_u32 s41, s28, s19
	v_readlane_b32 s19, v254, 25
	v_and_b32_e32 v2, 0xffff8000, v2
	s_addc_u32 s42, s19, s22
	v_lshl_add_u32 v2, v12, 11, v2
	v_and_b32_e32 v3, 1, v10
	v_readlane_b32 s19, v254, 13
	v_lshl_or_b32 v2, v3, 6, v2
	s_add_u32 s18, s19, s18
	v_readlane_b32 s19, v254, 14
	v_lshl_add_u32 v2, v13, 1, v2
	v_mov_b32_e32 v3, v99
	s_addc_u32 s19, s19, 0
	v_lshl_add_u64 v[134:135], s[18:19], 0, v[2:3]
	v_lshlrev_b32_e32 v2, 14, v11
	v_and_b32_e32 v2, 0xffff8000, v2
	v_lshl_add_u32 v2, v14, 11, v2
	v_and_b32_e32 v3, 1, v11
	v_lshl_or_b32 v2, v3, 6, v2
	v_lshl_add_u32 v2, v15, 1, v2
	v_mov_b32_e32 v3, v99
	v_lshl_add_u64 v[136:137], s[18:19], 0, v[2:3]
	v_mov_b32_e32 v2, 0
	s_mov_b32 s43, -2
	s_mov_b64 s[18:19], 0
	v_add_u32_e32 v140, 0, v18
	v_mov_b32_e32 v3, v2
	v_mov_b32_e32 v4, v2
	v_mov_b32_e32 v5, v2
	v_mov_b32_e32 v6, v2
	v_mov_b32_e32 v7, v2
	v_mov_b32_e32 v8, v2
	v_mov_b32_e32 v9, v2
	v_mov_b32_e32 v10, v2
	v_mov_b32_e32 v11, v2
	v_mov_b32_e32 v12, v2
	v_mov_b32_e32 v13, v2
	v_mov_b32_e32 v14, v2
	v_mov_b32_e32 v15, v2
	v_mov_b32_e32 v16, v2
	v_mov_b32_e32 v17, v2
	v_mov_b32_e32 v18, v2
	v_mov_b32_e32 v19, v2
	v_mov_b32_e32 v20, v2
	v_mov_b32_e32 v21, v2
	v_mov_b32_e32 v22, v2
	v_mov_b32_e32 v23, v2
	v_mov_b32_e32 v24, v2
	v_mov_b32_e32 v25, v2
	v_mov_b32_e32 v26, v2
	v_mov_b32_e32 v27, v2
	v_mov_b32_e32 v28, v2
	v_mov_b32_e32 v29, v2
	v_mov_b32_e32 v30, v2
	v_mov_b32_e32 v31, v2
	v_mov_b32_e32 v32, v2
	v_mov_b32_e32 v33, v2
	v_mov_b32_e32 v58, v2
	v_mov_b32_e32 v59, v2
	v_mov_b32_e32 v60, v2
	v_mov_b32_e32 v61, v2
	v_mov_b32_e32 v62, v2
	v_mov_b32_e32 v63, v2
	v_mov_b32_e32 v64, v2
	v_mov_b32_e32 v65, v2
	v_mov_b32_e32 v70, v2
	v_mov_b32_e32 v71, v2
	v_mov_b32_e32 v72, v2
	v_mov_b32_e32 v73, v2
	v_mov_b32_e32 v74, v2
	v_mov_b32_e32 v75, v2
	v_mov_b32_e32 v76, v2
	v_mov_b32_e32 v77, v2
	v_mov_b32_e32 v82, v2
	v_mov_b32_e32 v83, v2
	v_mov_b32_e32 v84, v2
	v_mov_b32_e32 v85, v2
	v_mov_b32_e32 v86, v2
	v_mov_b32_e32 v87, v2
	v_mov_b32_e32 v88, v2
	v_mov_b32_e32 v89, v2
	v_mov_b32_e32 v90, v2
	v_mov_b32_e32 v91, v2
	v_mov_b32_e32 v92, v2
	v_mov_b32_e32 v93, v2
	v_mov_b32_e32 v94, v2
	v_mov_b32_e32 v95, v2
	v_mov_b32_e32 v96, v2
	v_mov_b32_e32 v97, v2
	v_mov_b32_e32 v34, v2
	v_mov_b32_e32 v35, v2
	v_mov_b32_e32 v36, v2
	v_mov_b32_e32 v37, v2
	v_mov_b32_e32 v38, v2
	v_mov_b32_e32 v39, v2
	v_mov_b32_e32 v40, v2
	v_mov_b32_e32 v41, v2
	v_mov_b32_e32 v42, v2
	v_mov_b32_e32 v43, v2
	v_mov_b32_e32 v44, v2
	v_mov_b32_e32 v45, v2
	v_mov_b32_e32 v46, v2
	v_mov_b32_e32 v47, v2
	v_mov_b32_e32 v48, v2
	v_mov_b32_e32 v49, v2
	v_mov_b32_e32 v50, v2
	v_mov_b32_e32 v51, v2
	v_mov_b32_e32 v52, v2
	v_mov_b32_e32 v53, v2
	v_mov_b32_e32 v54, v2
	v_mov_b32_e32 v55, v2
	v_mov_b32_e32 v56, v2
	v_mov_b32_e32 v57, v2
	v_mov_b32_e32 v66, v2
	v_mov_b32_e32 v67, v2
	v_mov_b32_e32 v68, v2
	v_mov_b32_e32 v69, v2
	v_mov_b32_e32 v78, v2
	v_mov_b32_e32 v79, v2
	v_mov_b32_e32 v80, v2
	v_mov_b32_e32 v81, v2
	v_mov_b32_e32 v100, v2
	v_mov_b32_e32 v101, v2
	v_mov_b32_e32 v102, v2
	v_mov_b32_e32 v103, v2
	v_mov_b32_e32 v104, v2
	v_mov_b32_e32 v105, v2
	v_mov_b32_e32 v106, v2
	v_mov_b32_e32 v107, v2
	v_mov_b32_e32 v108, v2
	v_mov_b32_e32 v109, v2
	v_mov_b32_e32 v110, v2
	v_mov_b32_e32 v111, v2
	v_mov_b32_e32 v112, v2
	v_mov_b32_e32 v113, v2
	v_mov_b32_e32 v114, v2
	v_mov_b32_e32 v115, v2
	v_mov_b32_e32 v116, v2
	v_mov_b32_e32 v117, v2
	v_mov_b32_e32 v118, v2
	v_mov_b32_e32 v119, v2
	v_mov_b32_e32 v120, v2
	v_mov_b32_e32 v121, v2
	v_mov_b32_e32 v122, v2
	v_mov_b32_e32 v123, v2
	v_mov_b32_e32 v124, v2
	v_mov_b32_e32 v125, v2
	v_mov_b32_e32 v126, v2
	v_mov_b32_e32 v127, v2
	v_mov_b32_e32 v128, v2
	v_mov_b32_e32 v129, v2
	v_mov_b32_e32 v130, v2
	v_mov_b32_e32 v131, v2
	.p2alignl 6, 3212836864

.LBB0_2344:
	v_lshl_add_u64 v[24:25], v[12:13], 0, s[4:5]
	s_mov_b32 s3, 0x31d08000
	s_mov_b64 s[10:11], 0x31d08000
	v_add_co_u32_e32 v26, vcc, s3, v24
	v_lshl_add_u64 v[28:29], v[24:25], 0, s[10:11]
	s_nop 0
	v_addc_co_u32_e32 v27, vcc, 0, v25, vcc
	global_load_dwordx4 v[42:45], v[26:27], off
	global_load_dwordx4 v[46:49], v[28:29], off offset:16
	global_load_dwordx4 v[50:53], v[10:11], off offset:-496
	global_load_dwordx4 v[54:57], v[10:11], off offset:-512
	v_lshl_add_u64 v[28:29], v[18:19], 0, s[4:5]
	global_load_dwordx4 v[58:61], v[28:29], off offset:16
	global_load_dwordx4 v[62:65], v[28:29], off
	v_lshl_add_u64 v[30:31], v[16:17], 0, s[4:5]
	global_load_dwordx4 v[66:69], v[30:31], off offset:16
	global_load_dwordx4 v[70:73], v[30:31], off
	s_mov_b64 s[10:11], 0x31d08080
	v_lshl_add_u64 v[16:17], v[16:17], 0, s[14:15]
	v_lshl_add_u64 v[18:19], v[18:19], 0, s[14:15]
	v_lshl_add_u64 v[12:13], v[12:13], 0, s[14:15]
	s_waitcnt vmcnt(7)
	v_pk_mul_f32 v[32:33], v[22:23], v[44:45]
	v_pk_mul_f32 v[42:43], v[20:21], v[42:43]
	s_waitcnt vmcnt(4)
	v_pk_mul_f32 v[32:33], v[32:33], v[56:57]
	v_pk_mul_f32 v[42:43], v[42:43], v[54:55]
	s_waitcnt vmcnt(2)
	v_pk_add_f32 v[44:45], v[64:65], 1.0 op_sel_hi:[1,0]
	v_pk_add_f32 v[54:55], v[62:63], 1.0 op_sel_hi:[1,0]
	s_waitcnt vmcnt(0)
	v_pk_fma_f32 v[56:57], v[32:33], v[44:45], v[72:73]
	v_pk_mul_f32 v[44:45], v[20:21], v[46:47]
	v_pk_fma_f32 v[42:43], v[42:43], v[54:55], v[70:71]
	v_pk_mul_f32 v[32:33], v[22:23], v[48:49]
	v_pk_mul_f32 v[44:45], v[44:45], v[50:51]
	v_pk_add_f32 v[48:49], v[58:59], 1.0 op_sel_hi:[1,0]
	v_pk_mul_f32 v[32:33], v[32:33], v[52:53]
	v_pk_fma_f32 v[50:51], v[44:45], v[48:49], v[66:67]
	v_cvt_pk_bf16_f32 v44, v42, v43
	v_lshlrev_b32_e32 v48, 16, v44
	v_and_b32_e32 v49, 0xffff0000, v44
	v_cvt_pk_bf16_f32 v45, v56, v57
	v_pk_add_f32 v[42:43], v[42:43], v[48:49] neg_lo:[0,1] neg_hi:[0,1]
	v_pk_add_f32 v[46:47], v[60:61], 1.0 op_sel_hi:[1,0]
	v_cvt_pk_bf16_f32 v48, v42, v43
	v_lshlrev_b32_e32 v42, 16, v45
	v_and_b32_e32 v43, 0xffff0000, v45
	v_pk_fma_f32 v[52:53], v[32:33], v[46:47], v[68:69]
	v_cvt_pk_bf16_f32 v46, v50, v51
	v_pk_add_f32 v[42:43], v[56:57], v[42:43] neg_lo:[0,1] neg_hi:[0,1]
	v_cvt_pk_bf16_f32 v47, v52, v53
	v_cvt_pk_bf16_f32 v49, v42, v43
	v_lshlrev_b32_e32 v42, 16, v46
	v_and_b32_e32 v43, 0xffff0000, v46
	v_pk_add_f32 v[42:43], v[50:51], v[42:43] neg_lo:[0,1] neg_hi:[0,1]
	v_lshl_add_u64 v[32:33], v[14:15], 0, s[4:5]
	v_cvt_pk_bf16_f32 v50, v42, v43
	v_lshlrev_b32_e32 v42, 16, v47
	v_and_b32_e32 v43, 0xffff0000, v47
	v_pk_add_f32 v[42:43], v[52:53], v[42:43] neg_lo:[0,1] neg_hi:[0,1]
	global_store_dwordx4 v[32:33], v[44:47], off offset:-256
	v_cvt_pk_bf16_f32 v51, v42, v43
	v_add_u32_e32 v42, s2, v38
	v_xor_b32_e32 v43, v42, v37
	v_lshlrev_b32_e32 v43, 4, v43
	v_add_u32_e32 v60, v39, v43
	ds_read_b128 v[52:55], v60
	v_add_u32_e32 v56, v40, v43
	ds_read_b128 v[56:59], v56
	s_waitcnt lgkmcnt(1)
	v_mfma_f32_16x16x32_bf16 v[6:9], v[44:47], v[52:55], v[6:9]
	v_add_u32_e32 v43, v41, v43
	s_add_i32 s2, s2, 32
	s_cmpk_eq_i32 s2, 0x80
	v_mfma_f32_16x16x32_bf16 v[6:9], v[48:51], v[52:55], v[6:9]
	ds_read_b128 v[52:55], v60 offset:32768
	s_waitcnt lgkmcnt(1)
	v_mfma_f32_16x16x32_bf16 v[6:9], v[44:47], v[56:59], v[6:9]
	ds_read_b128 v[56:59], v43
	v_add_u32_e32 v43, 4, v42
	v_xor_b32_e32 v43, v43, v37
	s_waitcnt lgkmcnt(1)
	v_mfma_f32_16x16x32_bf16 v[2:5], v[44:47], v[52:55], v[2:5]
	v_lshlrev_b32_e32 v43, 4, v43
	v_mfma_f32_16x16x32_bf16 v[2:5], v[48:51], v[52:55], v[2:5]
	v_lshl_add_u64 v[48:49], v[24:25], 0, s[10:11]
	s_mov_b64 s[10:11], 0x31d08100
	s_waitcnt lgkmcnt(0)
	v_mfma_f32_16x16x32_bf16 v[2:5], v[44:47], v[56:59], v[2:5]
	global_load_dwordx4 v[44:47], v[26:27], off offset:128
	s_nop 0
	global_load_dwordx4 v[48:51], v[48:49], off offset:16
	s_nop 0
	global_load_dwordx4 v[52:55], v[10:11], off offset:-368
	global_load_dwordx4 v[56:59], v[10:11], off offset:-384
	global_load_dwordx4 v[60:63], v[28:29], off offset:144
	global_load_dwordx4 v[64:67], v[28:29], off offset:128
	global_load_dwordx4 v[68:71], v[30:31], off offset:144
	global_load_dwordx4 v[72:75], v[30:31], off offset:128
	s_waitcnt vmcnt(7)
	v_pk_mul_f32 v[46:47], v[22:23], v[46:47]
	v_pk_mul_f32 v[44:45], v[20:21], v[44:45]
	s_waitcnt vmcnt(4)
	v_pk_mul_f32 v[46:47], v[46:47], v[58:59]
	v_pk_mul_f32 v[44:45], v[44:45], v[56:57]
	s_waitcnt vmcnt(2)
	v_pk_add_f32 v[58:59], v[64:65], 1.0 op_sel_hi:[1,0]
	v_pk_add_f32 v[56:57], v[66:67], 1.0 op_sel_hi:[1,0]
	s_waitcnt vmcnt(0)
	v_pk_fma_f32 v[58:59], v[44:45], v[58:59], v[72:73]
	v_pk_mul_f32 v[44:45], v[22:23], v[50:51]
	v_pk_fma_f32 v[56:57], v[46:47], v[56:57], v[74:75]
	v_pk_mul_f32 v[46:47], v[20:21], v[48:49]
	v_pk_mul_f32 v[44:45], v[44:45], v[54:55]
	v_pk_add_f32 v[48:49], v[62:63], 1.0 op_sel_hi:[1,0]
	v_pk_mul_f32 v[46:47], v[46:47], v[52:53]
	v_pk_add_f32 v[50:51], v[60:61], 1.0 op_sel_hi:[1,0]
	v_pk_fma_f32 v[52:53], v[44:45], v[48:49], v[70:71]
	v_cvt_pk_bf16_f32 v44, v58, v59
	v_cvt_pk_bf16_f32 v45, v56, v57
	v_pk_fma_f32 v[50:51], v[46:47], v[50:51], v[68:69]
	v_lshlrev_b32_e32 v48, 16, v44
	v_and_b32_e32 v49, 0xffff0000, v44
	v_lshlrev_b32_e32 v54, 16, v45
	v_and_b32_e32 v55, 0xffff0000, v45
	v_cvt_pk_bf16_f32 v46, v50, v51
	v_pk_add_f32 v[48:49], v[58:59], v[48:49] neg_lo:[0,1] neg_hi:[0,1]
	v_pk_add_f32 v[54:55], v[56:57], v[54:55] neg_lo:[0,1] neg_hi:[0,1]
	v_cvt_pk_bf16_f32 v47, v52, v53
	v_cvt_pk_bf16_f32 v48, v48, v49
	v_cvt_pk_bf16_f32 v49, v54, v55
	v_lshlrev_b32_e32 v54, 16, v46
	v_and_b32_e32 v55, 0xffff0000, v46
	v_pk_add_f32 v[50:51], v[50:51], v[54:55] neg_lo:[0,1] neg_hi:[0,1]
	v_lshlrev_b32_e32 v54, 16, v47
	v_and_b32_e32 v55, 0xffff0000, v47
	v_pk_add_f32 v[52:53], v[52:53], v[54:55] neg_lo:[0,1] neg_hi:[0,1]
	v_add_u32_e32 v60, v39, v43
	v_cvt_pk_bf16_f32 v50, v50, v51
	v_cvt_pk_bf16_f32 v51, v52, v53
	ds_read_b128 v[52:55], v60
	v_add_u32_e32 v56, v40, v43
	ds_read_b128 v[56:59], v56
	s_waitcnt lgkmcnt(1)
	v_mfma_f32_16x16x32_bf16 v[6:9], v[44:47], v[52:55], v[6:9]
	v_add_u32_e32 v43, v41, v43
	global_store_dwordx4 v[32:33], v[44:47], off offset:-192
	v_mfma_f32_16x16x32_bf16 v[6:9], v[48:51], v[52:55], v[6:9]
	ds_read_b128 v[52:55], v60 offset:32768
	s_waitcnt lgkmcnt(1)
	v_mfma_f32_16x16x32_bf16 v[6:9], v[44:47], v[56:59], v[6:9]
	ds_read_b128 v[56:59], v43
	v_add_u32_e32 v43, 8, v42
	v_xor_b32_e32 v43, v43, v37
	s_waitcnt lgkmcnt(1)
	v_mfma_f32_16x16x32_bf16 v[2:5], v[44:47], v[52:55], v[2:5]
	v_lshlrev_b32_e32 v43, 4, v43
	v_mfma_f32_16x16x32_bf16 v[2:5], v[48:51], v[52:55], v[2:5]
	v_lshl_add_u64 v[48:49], v[24:25], 0, s[10:11]
	s_mov_b64 s[10:11], 0x31d08180
	s_waitcnt lgkmcnt(0)
	v_mfma_f32_16x16x32_bf16 v[2:5], v[44:47], v[56:59], v[2:5]
	global_load_dwordx4 v[44:47], v[26:27], off offset:256
	s_nop 0
	global_load_dwordx4 v[48:51], v[48:49], off offset:16
	s_nop 0
	global_load_dwordx4 v[52:55], v[10:11], off offset:-240
	global_load_dwordx4 v[56:59], v[10:11], off offset:-256
	global_load_dwordx4 v[60:63], v[28:29], off offset:272
	global_load_dwordx4 v[64:67], v[28:29], off offset:256
	global_load_dwordx4 v[68:71], v[30:31], off offset:272
	global_load_dwordx4 v[72:75], v[30:31], off offset:256
	s_waitcnt vmcnt(7)
	v_pk_mul_f32 v[46:47], v[22:23], v[46:47]
	v_pk_mul_f32 v[44:45], v[20:21], v[44:45]
	s_waitcnt vmcnt(4)
	v_pk_mul_f32 v[46:47], v[46:47], v[58:59]
	v_pk_mul_f32 v[44:45], v[44:45], v[56:57]
	s_waitcnt vmcnt(2)
	v_pk_add_f32 v[58:59], v[64:65], 1.0 op_sel_hi:[1,0]
	v_pk_add_f32 v[56:57], v[66:67], 1.0 op_sel_hi:[1,0]
	s_waitcnt vmcnt(0)
	v_pk_fma_f32 v[58:59], v[44:45], v[58:59], v[72:73]
	v_pk_mul_f32 v[44:45], v[22:23], v[50:51]
	v_pk_fma_f32 v[56:57], v[46:47], v[56:57], v[74:75]
	v_pk_mul_f32 v[46:47], v[20:21], v[48:49]
	v_pk_mul_f32 v[44:45], v[44:45], v[54:55]
	v_pk_add_f32 v[48:49], v[62:63], 1.0 op_sel_hi:[1,0]
	v_pk_mul_f32 v[46:47], v[46:47], v[52:53]
	v_pk_add_f32 v[50:51], v[60:61], 1.0 op_sel_hi:[1,0]
	v_pk_fma_f32 v[52:53], v[44:45], v[48:49], v[70:71]
	v_cvt_pk_bf16_f32 v44, v58, v59
	v_cvt_pk_bf16_f32 v45, v56, v57
	v_pk_fma_f32 v[50:51], v[46:47], v[50:51], v[68:69]
	v_lshlrev_b32_e32 v48, 16, v44
	v_and_b32_e32 v49, 0xffff0000, v44
	v_lshlrev_b32_e32 v54, 16, v45
	v_and_b32_e32 v55, 0xffff0000, v45
	v_cvt_pk_bf16_f32 v46, v50, v51
	v_pk_add_f32 v[48:49], v[58:59], v[48:49] neg_lo:[0,1] neg_hi:[0,1]
	v_pk_add_f32 v[54:55], v[56:57], v[54:55] neg_lo:[0,1] neg_hi:[0,1]
	v_cvt_pk_bf16_f32 v47, v52, v53
	v_cvt_pk_bf16_f32 v48, v48, v49
	v_cvt_pk_bf16_f32 v49, v54, v55
	v_lshlrev_b32_e32 v54, 16, v46
	v_and_b32_e32 v55, 0xffff0000, v46
	v_pk_add_f32 v[50:51], v[50:51], v[54:55] neg_lo:[0,1] neg_hi:[0,1]
	v_lshlrev_b32_e32 v54, 16, v47
	v_and_b32_e32 v55, 0xffff0000, v47
	v_pk_add_f32 v[52:53], v[52:53], v[54:55] neg_lo:[0,1] neg_hi:[0,1]
	v_add_u32_e32 v60, v39, v43
	v_cvt_pk_bf16_f32 v50, v50, v51
	v_cvt_pk_bf16_f32 v51, v52, v53
	ds_read_b128 v[52:55], v60
	v_add_u32_e32 v56, v40, v43
	ds_read_b128 v[56:59], v56
	s_waitcnt lgkmcnt(1)
	v_mfma_f32_16x16x32_bf16 v[6:9], v[44:47], v[52:55], v[6:9]
	v_add_u32_e32 v43, v41, v43
	global_store_dwordx4 v[32:33], v[44:47], off offset:-128
	v_mfma_f32_16x16x32_bf16 v[6:9], v[48:51], v[52:55], v[6:9]
	ds_read_b128 v[52:55], v60 offset:32768
	s_waitcnt lgkmcnt(1)
	v_mfma_f32_16x16x32_bf16 v[6:9], v[44:47], v[56:59], v[6:9]
	ds_read_b128 v[56:59], v43
	v_add_u32_e32 v43, 12, v42
	v_xor_b32_e32 v43, v43, v37
	s_waitcnt lgkmcnt(1)
	v_mfma_f32_16x16x32_bf16 v[2:5], v[44:47], v[52:55], v[2:5]
	v_lshlrev_b32_e32 v43, 4, v43
	v_mfma_f32_16x16x32_bf16 v[2:5], v[48:51], v[52:55], v[2:5]
	v_lshl_add_u64 v[48:49], v[24:25], 0, s[10:11]
	s_mov_b64 s[10:11], 0x31d08200
	s_waitcnt lgkmcnt(0)
	v_mfma_f32_16x16x32_bf16 v[2:5], v[44:47], v[56:59], v[2:5]
	global_load_dwordx4 v[44:47], v[26:27], off offset:384
	s_nop 0
	global_load_dwordx4 v[48:51], v[48:49], off offset:16
	s_nop 0
	global_load_dwordx4 v[52:55], v[10:11], off offset:-112
	global_load_dwordx4 v[56:59], v[10:11], off offset:-128
	global_load_dwordx4 v[60:63], v[28:29], off offset:400
	global_load_dwordx4 v[64:67], v[28:29], off offset:384
	global_load_dwordx4 v[68:71], v[30:31], off offset:400
	global_load_dwordx4 v[72:75], v[30:31], off offset:384
	s_waitcnt vmcnt(7)
	v_pk_mul_f32 v[46:47], v[22:23], v[46:47]
	v_pk_mul_f32 v[44:45], v[20:21], v[44:45]
	s_waitcnt vmcnt(4)
	v_pk_mul_f32 v[46:47], v[46:47], v[58:59]
	v_pk_mul_f32 v[44:45], v[44:45], v[56:57]
	s_waitcnt vmcnt(2)
	v_pk_add_f32 v[58:59], v[64:65], 1.0 op_sel_hi:[1,0]
	v_pk_add_f32 v[56:57], v[66:67], 1.0 op_sel_hi:[1,0]
	s_waitcnt vmcnt(0)
	v_pk_fma_f32 v[58:59], v[44:45], v[58:59], v[72:73]
	v_pk_mul_f32 v[44:45], v[22:23], v[50:51]
	v_pk_fma_f32 v[56:57], v[46:47], v[56:57], v[74:75]
	v_pk_mul_f32 v[46:47], v[20:21], v[48:49]
	v_pk_mul_f32 v[44:45], v[44:45], v[54:55]
	v_pk_add_f32 v[48:49], v[62:63], 1.0 op_sel_hi:[1,0]
	v_pk_mul_f32 v[46:47], v[46:47], v[52:53]
	v_pk_add_f32 v[50:51], v[60:61], 1.0 op_sel_hi:[1,0]
	v_pk_fma_f32 v[52:53], v[44:45], v[48:49], v[70:71]
	v_cvt_pk_bf16_f32 v44, v58, v59
	v_cvt_pk_bf16_f32 v45, v56, v57
	v_pk_fma_f32 v[50:51], v[46:47], v[50:51], v[68:69]
	v_lshlrev_b32_e32 v48, 16, v44
	v_and_b32_e32 v49, 0xffff0000, v44
	v_lshlrev_b32_e32 v54, 16, v45
	v_and_b32_e32 v55, 0xffff0000, v45
	v_cvt_pk_bf16_f32 v46, v50, v51
	v_pk_add_f32 v[48:49], v[58:59], v[48:49] neg_lo:[0,1] neg_hi:[0,1]
	v_pk_add_f32 v[54:55], v[56:57], v[54:55] neg_lo:[0,1] neg_hi:[0,1]
	v_cvt_pk_bf16_f32 v47, v52, v53
	v_cvt_pk_bf16_f32 v48, v48, v49
	v_cvt_pk_bf16_f32 v49, v54, v55
	v_lshlrev_b32_e32 v54, 16, v46
	v_and_b32_e32 v55, 0xffff0000, v46
	v_pk_add_f32 v[50:51], v[50:51], v[54:55] neg_lo:[0,1] neg_hi:[0,1]
	v_lshlrev_b32_e32 v54, 16, v47
	v_and_b32_e32 v55, 0xffff0000, v47
	v_pk_add_f32 v[52:53], v[52:53], v[54:55] neg_lo:[0,1] neg_hi:[0,1]
	v_add_u32_e32 v60, v39, v43
	v_cvt_pk_bf16_f32 v50, v50, v51
	v_cvt_pk_bf16_f32 v51, v52, v53
	ds_read_b128 v[52:55], v60
	v_add_u32_e32 v56, v40, v43
	ds_read_b128 v[56:59], v56
	s_waitcnt lgkmcnt(1)
	v_mfma_f32_16x16x32_bf16 v[6:9], v[44:47], v[52:55], v[6:9]
	v_add_u32_e32 v43, v41, v43
	global_store_dwordx4 v[32:33], v[44:47], off offset:-64
	v_mfma_f32_16x16x32_bf16 v[6:9], v[48:51], v[52:55], v[6:9]
	ds_read_b128 v[52:55], v60 offset:32768
	s_waitcnt lgkmcnt(1)
	v_mfma_f32_16x16x32_bf16 v[6:9], v[44:47], v[56:59], v[6:9]
	ds_read_b128 v[56:59], v43
	v_add_u32_e32 v43, 16, v42
	v_xor_b32_e32 v43, v43, v37
	s_waitcnt lgkmcnt(1)
	v_mfma_f32_16x16x32_bf16 v[2:5], v[44:47], v[52:55], v[2:5]
	v_lshlrev_b32_e32 v43, 4, v43
	v_mfma_f32_16x16x32_bf16 v[2:5], v[48:51], v[52:55], v[2:5]
	v_lshl_add_u64 v[48:49], v[24:25], 0, s[10:11]
	s_mov_b64 s[10:11], 0x31d08280
	s_waitcnt lgkmcnt(0)
	v_mfma_f32_16x16x32_bf16 v[2:5], v[44:47], v[56:59], v[2:5]
	global_load_dwordx4 v[44:47], v[26:27], off offset:512
	s_nop 0
	global_load_dwordx4 v[48:51], v[48:49], off offset:16
	s_nop 0
	global_load_dwordx4 v[52:55], v[10:11], off offset:16
	global_load_dwordx4 v[56:59], v[10:11], off
	global_load_dwordx4 v[60:63], v[28:29], off offset:528
	global_load_dwordx4 v[64:67], v[28:29], off offset:512
	global_load_dwordx4 v[68:71], v[30:31], off offset:528
	global_load_dwordx4 v[72:75], v[30:31], off offset:512
	s_waitcnt vmcnt(7)
	v_pk_mul_f32 v[46:47], v[22:23], v[46:47]
	v_pk_mul_f32 v[44:45], v[20:21], v[44:45]
	s_waitcnt vmcnt(4)
	v_pk_mul_f32 v[46:47], v[46:47], v[58:59]
	v_pk_mul_f32 v[44:45], v[44:45], v[56:57]
	s_waitcnt vmcnt(2)
	v_pk_add_f32 v[58:59], v[64:65], 1.0 op_sel_hi:[1,0]
	v_pk_add_f32 v[56:57], v[66:67], 1.0 op_sel_hi:[1,0]
	s_waitcnt vmcnt(0)
	v_pk_fma_f32 v[58:59], v[44:45], v[58:59], v[72:73]
	v_pk_mul_f32 v[44:45], v[22:23], v[50:51]
	v_pk_fma_f32 v[56:57], v[46:47], v[56:57], v[74:75]
	v_pk_mul_f32 v[46:47], v[20:21], v[48:49]
	v_pk_mul_f32 v[44:45], v[44:45], v[54:55]
	v_pk_add_f32 v[48:49], v[62:63], 1.0 op_sel_hi:[1,0]
	v_pk_mul_f32 v[46:47], v[46:47], v[52:53]
	v_pk_add_f32 v[50:51], v[60:61], 1.0 op_sel_hi:[1,0]
	v_pk_fma_f32 v[52:53], v[44:45], v[48:49], v[70:71]
	v_cvt_pk_bf16_f32 v44, v58, v59
	v_cvt_pk_bf16_f32 v45, v56, v57
	v_pk_fma_f32 v[50:51], v[46:47], v[50:51], v[68:69]
	v_lshlrev_b32_e32 v48, 16, v44
	v_and_b32_e32 v49, 0xffff0000, v44
	v_lshlrev_b32_e32 v54, 16, v45
	v_and_b32_e32 v55, 0xffff0000, v45
	v_cvt_pk_bf16_f32 v46, v50, v51
	v_pk_add_f32 v[48:49], v[58:59], v[48:49] neg_lo:[0,1] neg_hi:[0,1]
	v_pk_add_f32 v[54:55], v[56:57], v[54:55] neg_lo:[0,1] neg_hi:[0,1]
	v_cvt_pk_bf16_f32 v47, v52, v53
	v_cvt_pk_bf16_f32 v48, v48, v49
	v_cvt_pk_bf16_f32 v49, v54, v55
	v_lshlrev_b32_e32 v54, 16, v46
	v_and_b32_e32 v55, 0xffff0000, v46
	v_pk_add_f32 v[50:51], v[50:51], v[54:55] neg_lo:[0,1] neg_hi:[0,1]
	v_lshlrev_b32_e32 v54, 16, v47
	v_and_b32_e32 v55, 0xffff0000, v47
	v_pk_add_f32 v[52:53], v[52:53], v[54:55] neg_lo:[0,1] neg_hi:[0,1]
	v_add_u32_e32 v60, v39, v43
	v_cvt_pk_bf16_f32 v50, v50, v51
	v_cvt_pk_bf16_f32 v51, v52, v53
	ds_read_b128 v[52:55], v60
	v_add_u32_e32 v56, v40, v43
	ds_read_b128 v[56:59], v56
	s_waitcnt lgkmcnt(1)
	v_mfma_f32_16x16x32_bf16 v[6:9], v[44:47], v[52:55], v[6:9]
	v_add_u32_e32 v43, v41, v43
	global_store_dwordx4 v[32:33], v[44:47], off
	v_mfma_f32_16x16x32_bf16 v[6:9], v[48:51], v[52:55], v[6:9]
	ds_read_b128 v[52:55], v60 offset:32768
	s_waitcnt lgkmcnt(1)
	v_mfma_f32_16x16x32_bf16 v[6:9], v[44:47], v[56:59], v[6:9]
	ds_read_b128 v[56:59], v43
	v_add_u32_e32 v43, 20, v42
	v_xor_b32_e32 v43, v43, v37
	s_waitcnt lgkmcnt(1)
	v_mfma_f32_16x16x32_bf16 v[2:5], v[44:47], v[52:55], v[2:5]
	v_lshlrev_b32_e32 v43, 4, v43
	v_mfma_f32_16x16x32_bf16 v[2:5], v[48:51], v[52:55], v[2:5]
	v_lshl_add_u64 v[48:49], v[24:25], 0, s[10:11]
	s_mov_b64 s[10:11], 0x31d08300
	s_waitcnt lgkmcnt(0)
	v_mfma_f32_16x16x32_bf16 v[2:5], v[44:47], v[56:59], v[2:5]
	global_load_dwordx4 v[44:47], v[26:27], off offset:640
	s_nop 0
	global_load_dwordx4 v[48:51], v[48:49], off offset:16
	s_nop 0
	global_load_dwordx4 v[52:55], v[10:11], off offset:144
	global_load_dwordx4 v[56:59], v[10:11], off offset:128
	global_load_dwordx4 v[60:63], v[28:29], off offset:656
	global_load_dwordx4 v[64:67], v[28:29], off offset:640
	global_load_dwordx4 v[68:71], v[30:31], off offset:656
	global_load_dwordx4 v[72:75], v[30:31], off offset:640
	s_waitcnt vmcnt(7)
	v_pk_mul_f32 v[46:47], v[22:23], v[46:47]
	v_pk_mul_f32 v[44:45], v[20:21], v[44:45]
	s_waitcnt vmcnt(4)
	v_pk_mul_f32 v[46:47], v[46:47], v[58:59]
	v_pk_mul_f32 v[44:45], v[44:45], v[56:57]
	s_waitcnt vmcnt(2)
	v_pk_add_f32 v[58:59], v[64:65], 1.0 op_sel_hi:[1,0]
	v_pk_add_f32 v[56:57], v[66:67], 1.0 op_sel_hi:[1,0]
	s_waitcnt vmcnt(0)
	v_pk_fma_f32 v[58:59], v[44:45], v[58:59], v[72:73]
	v_pk_mul_f32 v[44:45], v[22:23], v[50:51]
	v_pk_fma_f32 v[56:57], v[46:47], v[56:57], v[74:75]
	v_pk_mul_f32 v[46:47], v[20:21], v[48:49]
	v_pk_mul_f32 v[44:45], v[44:45], v[54:55]
	v_pk_add_f32 v[48:49], v[62:63], 1.0 op_sel_hi:[1,0]
	v_pk_mul_f32 v[46:47], v[46:47], v[52:53]
	v_pk_add_f32 v[50:51], v[60:61], 1.0 op_sel_hi:[1,0]
	v_pk_fma_f32 v[52:53], v[44:45], v[48:49], v[70:71]
	v_cvt_pk_bf16_f32 v44, v58, v59
	v_cvt_pk_bf16_f32 v45, v56, v57
	v_pk_fma_f32 v[50:51], v[46:47], v[50:51], v[68:69]
	v_lshlrev_b32_e32 v48, 16, v44
	v_and_b32_e32 v49, 0xffff0000, v44
	v_lshlrev_b32_e32 v54, 16, v45
	v_and_b32_e32 v55, 0xffff0000, v45
	v_cvt_pk_bf16_f32 v46, v50, v51
	v_pk_add_f32 v[48:49], v[58:59], v[48:49] neg_lo:[0,1] neg_hi:[0,1]
	v_pk_add_f32 v[54:55], v[56:57], v[54:55] neg_lo:[0,1] neg_hi:[0,1]
	v_cvt_pk_bf16_f32 v47, v52, v53
	v_cvt_pk_bf16_f32 v48, v48, v49
	v_cvt_pk_bf16_f32 v49, v54, v55
	v_lshlrev_b32_e32 v54, 16, v46
	v_and_b32_e32 v55, 0xffff0000, v46
	v_pk_add_f32 v[50:51], v[50:51], v[54:55] neg_lo:[0,1] neg_hi:[0,1]
	v_lshlrev_b32_e32 v54, 16, v47
	v_and_b32_e32 v55, 0xffff0000, v47
	v_pk_add_f32 v[52:53], v[52:53], v[54:55] neg_lo:[0,1] neg_hi:[0,1]
	v_add_u32_e32 v60, v39, v43
	v_cvt_pk_bf16_f32 v50, v50, v51
	v_cvt_pk_bf16_f32 v51, v52, v53
	ds_read_b128 v[52:55], v60
	v_add_u32_e32 v56, v40, v43
	ds_read_b128 v[56:59], v56
	s_waitcnt lgkmcnt(1)
	v_mfma_f32_16x16x32_bf16 v[6:9], v[44:47], v[52:55], v[6:9]
	v_add_u32_e32 v43, v41, v43
	global_store_dwordx4 v[32:33], v[44:47], off offset:64
	v_mfma_f32_16x16x32_bf16 v[6:9], v[48:51], v[52:55], v[6:9]
	ds_read_b128 v[52:55], v60 offset:32768
	s_waitcnt lgkmcnt(1)
	v_mfma_f32_16x16x32_bf16 v[6:9], v[44:47], v[56:59], v[6:9]
	ds_read_b128 v[56:59], v43
	v_add_u32_e32 v43, 24, v42
	v_xor_b32_e32 v43, v43, v37
	s_waitcnt lgkmcnt(1)
	v_mfma_f32_16x16x32_bf16 v[2:5], v[44:47], v[52:55], v[2:5]
	v_lshlrev_b32_e32 v43, 4, v43
	v_mfma_f32_16x16x32_bf16 v[2:5], v[48:51], v[52:55], v[2:5]
	v_lshl_add_u64 v[48:49], v[24:25], 0, s[10:11]
	s_mov_b64 s[10:11], 0x31d08380
	s_waitcnt lgkmcnt(0)
	v_mfma_f32_16x16x32_bf16 v[2:5], v[44:47], v[56:59], v[2:5]
	global_load_dwordx4 v[44:47], v[26:27], off offset:768
	s_nop 0
	global_load_dwordx4 v[48:51], v[48:49], off offset:16
	s_nop 0
	global_load_dwordx4 v[52:55], v[10:11], off offset:272
	global_load_dwordx4 v[56:59], v[10:11], off offset:256
	global_load_dwordx4 v[60:63], v[28:29], off offset:784
	global_load_dwordx4 v[64:67], v[28:29], off offset:768
	global_load_dwordx4 v[68:71], v[30:31], off offset:784
	global_load_dwordx4 v[72:75], v[30:31], off offset:768
	s_waitcnt vmcnt(7)
	v_pk_mul_f32 v[46:47], v[22:23], v[46:47]
	v_pk_mul_f32 v[44:45], v[20:21], v[44:45]
	s_waitcnt vmcnt(4)
	v_pk_mul_f32 v[46:47], v[46:47], v[58:59]
	v_pk_mul_f32 v[44:45], v[44:45], v[56:57]
	s_waitcnt vmcnt(2)
	v_pk_add_f32 v[58:59], v[64:65], 1.0 op_sel_hi:[1,0]
	v_pk_add_f32 v[56:57], v[66:67], 1.0 op_sel_hi:[1,0]
	s_waitcnt vmcnt(0)
	v_pk_fma_f32 v[58:59], v[44:45], v[58:59], v[72:73]
	v_pk_mul_f32 v[44:45], v[22:23], v[50:51]
	v_pk_fma_f32 v[56:57], v[46:47], v[56:57], v[74:75]
	v_pk_mul_f32 v[46:47], v[20:21], v[48:49]
	v_pk_mul_f32 v[44:45], v[44:45], v[54:55]
	v_pk_add_f32 v[48:49], v[62:63], 1.0 op_sel_hi:[1,0]
	v_pk_mul_f32 v[46:47], v[46:47], v[52:53]
	v_pk_add_f32 v[50:51], v[60:61], 1.0 op_sel_hi:[1,0]
	v_pk_fma_f32 v[52:53], v[44:45], v[48:49], v[70:71]
	v_cvt_pk_bf16_f32 v44, v58, v59
	v_cvt_pk_bf16_f32 v45, v56, v57
	v_pk_fma_f32 v[50:51], v[46:47], v[50:51], v[68:69]
	v_lshlrev_b32_e32 v48, 16, v44
	v_and_b32_e32 v49, 0xffff0000, v44
	v_lshlrev_b32_e32 v54, 16, v45
	v_and_b32_e32 v55, 0xffff0000, v45
	v_cvt_pk_bf16_f32 v46, v50, v51
	v_pk_add_f32 v[48:49], v[58:59], v[48:49] neg_lo:[0,1] neg_hi:[0,1]
	v_pk_add_f32 v[54:55], v[56:57], v[54:55] neg_lo:[0,1] neg_hi:[0,1]
	v_cvt_pk_bf16_f32 v47, v52, v53
	v_cvt_pk_bf16_f32 v48, v48, v49
	v_cvt_pk_bf16_f32 v49, v54, v55
	v_lshlrev_b32_e32 v54, 16, v46
	v_and_b32_e32 v55, 0xffff0000, v46
	v_pk_add_f32 v[50:51], v[50:51], v[54:55] neg_lo:[0,1] neg_hi:[0,1]
	v_lshlrev_b32_e32 v54, 16, v47
	v_and_b32_e32 v55, 0xffff0000, v47
	v_pk_add_f32 v[52:53], v[52:53], v[54:55] neg_lo:[0,1] neg_hi:[0,1]
	v_add_u32_e32 v60, v39, v43
	v_cvt_pk_bf16_f32 v50, v50, v51
	v_cvt_pk_bf16_f32 v51, v52, v53
	ds_read_b128 v[52:55], v60
	v_add_u32_e32 v56, v40, v43
	ds_read_b128 v[56:59], v56
	s_waitcnt lgkmcnt(1)
	v_mfma_f32_16x16x32_bf16 v[6:9], v[44:47], v[52:55], v[6:9]
	v_add_u32_e32 v43, v41, v43
	global_store_dwordx4 v[32:33], v[44:47], off offset:128
	v_mfma_f32_16x16x32_bf16 v[6:9], v[48:51], v[52:55], v[6:9]
	ds_read_b128 v[52:55], v60 offset:32768
	s_waitcnt lgkmcnt(1)
	v_mfma_f32_16x16x32_bf16 v[6:9], v[44:47], v[56:59], v[6:9]
	ds_read_b128 v[56:59], v43
	s_waitcnt lgkmcnt(1)
	v_mfma_f32_16x16x32_bf16 v[2:5], v[44:47], v[52:55], v[2:5]
	v_mfma_f32_16x16x32_bf16 v[2:5], v[48:51], v[52:55], v[2:5]
	s_waitcnt lgkmcnt(0)
	v_mfma_f32_16x16x32_bf16 v[2:5], v[44:47], v[56:59], v[2:5]
	v_lshl_add_u64 v[44:45], v[24:25], 0, s[10:11]
	global_load_dwordx4 v[24:27], v[26:27], off offset:896
	s_nop 0
	global_load_dwordx4 v[44:47], v[44:45], off offset:16
	s_nop 0
	global_load_dwordx4 v[48:51], v[10:11], off offset:400
	global_load_dwordx4 v[52:55], v[10:11], off offset:384
	global_load_dwordx4 v[56:59], v[28:29], off offset:912
	global_load_dwordx4 v[60:63], v[28:29], off offset:896
	global_load_dwordx4 v[64:67], v[30:31], off offset:912
	s_nop 0
	global_load_dwordx4 v[28:31], v[30:31], off offset:896
	s_mov_b64 s[10:11], 0x200
	v_lshl_add_u64 v[10:11], v[10:11], 0, s[14:15]
	v_lshl_add_u64 v[14:15], v[14:15], 0, s[10:11]
	s_waitcnt vmcnt(7)
	v_pk_mul_f32 v[26:27], v[22:23], v[26:27]
	v_pk_mul_f32 v[24:25], v[20:21], v[24:25]
	s_waitcnt vmcnt(4)
	v_pk_mul_f32 v[26:27], v[26:27], v[54:55]
	v_pk_mul_f32 v[24:25], v[24:25], v[52:53]
	s_waitcnt vmcnt(2)
	v_pk_add_f32 v[52:53], v[62:63], 1.0 op_sel_hi:[1,0]
	v_pk_add_f32 v[54:55], v[60:61], 1.0 op_sel_hi:[1,0]
	s_waitcnt vmcnt(0)
	v_pk_fma_f32 v[30:31], v[26:27], v[52:53], v[30:31]
	v_pk_fma_f32 v[28:29], v[24:25], v[54:55], v[28:29]
	v_pk_mul_f32 v[24:25], v[22:23], v[46:47]
	v_pk_mul_f32 v[26:27], v[20:21], v[44:45]
	v_pk_mul_f32 v[24:25], v[24:25], v[50:51]
	v_pk_mul_f32 v[26:27], v[26:27], v[48:49]
	v_pk_add_f32 v[44:45], v[58:59], 1.0 op_sel_hi:[1,0]
	v_pk_add_f32 v[46:47], v[56:57], 1.0 op_sel_hi:[1,0]
	v_pk_fma_f32 v[44:45], v[24:25], v[44:45], v[66:67]
	v_pk_fma_f32 v[46:47], v[26:27], v[46:47], v[64:65]
	v_cvt_pk_bf16_f32 v24, v28, v29
	v_cvt_pk_bf16_f32 v25, v30, v31
	v_cvt_pk_bf16_f32 v26, v46, v47
	v_cvt_pk_bf16_f32 v27, v44, v45
	global_store_dwordx4 v[32:33], v[24:27], off offset:192
	v_lshlrev_b32_e32 v32, 16, v24
	v_and_b32_e32 v33, 0xffff0000, v24
	v_pk_add_f32 v[28:29], v[28:29], v[32:33] neg_lo:[0,1] neg_hi:[0,1]
	v_lshlrev_b32_e32 v32, 16, v25
	v_and_b32_e32 v33, 0xffff0000, v25
	v_pk_add_f32 v[30:31], v[30:31], v[32:33] neg_lo:[0,1] neg_hi:[0,1]
	v_cvt_pk_bf16_f32 v28, v28, v29
	v_cvt_pk_bf16_f32 v29, v30, v31
	v_lshlrev_b32_e32 v30, 16, v26
	v_and_b32_e32 v31, 0xffff0000, v26
	v_lshlrev_b32_e32 v32, 16, v27
	v_and_b32_e32 v33, 0xffff0000, v27
	v_pk_add_f32 v[30:31], v[46:47], v[30:31] neg_lo:[0,1] neg_hi:[0,1]
	v_pk_add_f32 v[32:33], v[44:45], v[32:33] neg_lo:[0,1] neg_hi:[0,1]
	v_cvt_pk_bf16_f32 v30, v30, v31
	v_cvt_pk_bf16_f32 v31, v32, v33
	v_add_u32_e32 v32, 28, v42
	v_xor_b32_e32 v32, v32, v37
	v_lshlrev_b32_e32 v32, 4, v32
	v_add_u32_e32 v33, v39, v32
	ds_read_b128 v[42:45], v33
	v_add_u32_e32 v46, v40, v32
	ds_read_b128 v[46:49], v46
	s_waitcnt lgkmcnt(1)
	v_mfma_f32_16x16x32_bf16 v[6:9], v[24:27], v[42:45], v[6:9]
	v_add_u32_e32 v32, v41, v32
	v_mfma_f32_16x16x32_bf16 v[6:9], v[28:31], v[42:45], v[6:9]
	ds_read_b128 v[42:45], v33 offset:32768
	s_waitcnt lgkmcnt(1)
	v_mfma_f32_16x16x32_bf16 v[6:9], v[24:27], v[46:49], v[6:9]
	ds_read_b128 v[46:49], v32
	s_waitcnt lgkmcnt(1)
	v_mfma_f32_16x16x32_bf16 v[2:5], v[24:27], v[42:45], v[2:5]
	v_mfma_f32_16x16x32_bf16 v[2:5], v[28:31], v[42:45], v[2:5]
	s_waitcnt lgkmcnt(0)
	v_mfma_f32_16x16x32_bf16 v[2:5], v[24:27], v[46:49], v[2:5]
	s_cbranch_scc0 .LBB0_2344
	v_readlane_b32 s52, v251, 54
	s_lshl_b32 s4, s86, 5
	v_readlane_b32 s58, v251, 60
	v_readlane_b32 s59, v251, 61
	s_lshl_b32 s14, s13, 11
	s_lshl_b64 s[2:3], s[4:5], 2
	s_mov_b64 s[50:51], s[58:59]
	s_add_u32 s10, s50, s2
	s_addc_u32 s11, s51, s3
	s_add_i32 s2, s14, 0
	s_add_i32 s2, s2, 0x20000
	v_lshlrev_b32_e32 v10, 2, v37
	v_lshlrev_b32_e32 v12, 9, v38
	global_load_dword v11, v10, s[10:11]
	v_add3_u32 v12, s2, v10, v12
	global_load_dword v10, v10, s[10:11] offset:64
	v_cmp_gt_u32_e32 vcc, 16, v35
	v_readlane_b32 s53, v251, 55
	v_readlane_b32 s54, v251, 56
	v_readlane_b32 s55, v251, 57
	v_readlane_b32 s56, v251, 58
	v_readlane_b32 s57, v251, 59
	v_readlane_b32 s60, v251, 62
	v_readlane_b32 s61, v251, 63
	v_readlane_b32 s62, v252, 0
	v_readlane_b32 s63, v252, 1
	v_readlane_b32 s64, v252, 2
	v_readlane_b32 s65, v252, 3
	v_readlane_b32 s66, v252, 4
	v_readlane_b32 s67, v252, 5
	s_waitcnt vmcnt(1)
	v_add_f32_e32 v6, v6, v11
	v_add_f32_e32 v7, v7, v11
	s_waitcnt vmcnt(0)
	v_add_f32_e32 v2, v2, v10
	ds_write2_b32 v12, v6, v2 offset1:16
	v_add_f32_e32 v2, v3, v10
	v_add_f32_e32 v8, v8, v11
	ds_write2_b32 v12, v7, v2 offset0:32 offset1:48
	v_add_f32_e32 v2, v4, v10
	v_add_f32_e32 v9, v9, v11
	ds_write2_b32 v12, v8, v2 offset0:64 offset1:80
	v_add_f32_e32 v2, v5, v10
	ds_write2_b32 v12, v9, v2 offset0:96 offset1:112
	s_waitcnt lgkmcnt(0)
	s_and_saveexec_b64 s[10:11], vcc
	s_cbranch_execz .LBB0_2347
	v_lshl_add_u32 v30, v35, 7, s2
	ds_read_b128 v[22:25], v30
	ds_read_b128 v[14:17], v30 offset:16
	ds_read_b128 v[6:9], v30 offset:32
	ds_read_b128 v[2:5], v30 offset:48
	s_lshl_b32 s3, s13, 8
	s_waitcnt lgkmcnt(3)
	v_max_f32_e32 v10, v22, v22
	s_add_i32 s3, s3, 0
	s_mov_b32 s2, 0xff61b1e6
	v_max_f32_e32 v10, 0xff61b1e6, v10
	v_lshl_add_u32 v37, v35, 4, s3
	v_cmp_lt_f32_e32 vcc, s2, v22
	v_cmp_gt_f32_e64 s[2:3], v23, v10
	v_mov_b32_e32 v48, 0xff61b1e6
	s_nop 0
	v_cndmask_b32_e64 v10, v10, v23, s[2:3]
	v_cndmask_b32_e64 v11, 0, 1, s[2:3]
	v_cmp_gt_f32_e64 s[2:3], v24, v10
	s_nop 1
	v_cndmask_b32_e64 v10, v10, v24, s[2:3]
	v_cndmask_b32_e64 v11, v11, 2, s[2:3]
	v_cmp_gt_f32_e64 s[2:3], v25, v10
	s_nop 1
	v_cndmask_b32_e64 v10, v10, v25, s[2:3]
	v_cndmask_b32_e64 v11, v11, 3, s[2:3]
	s_waitcnt lgkmcnt(2)
	v_cmp_gt_f32_e64 s[2:3], v14, v10
	s_nop 1
	v_cndmask_b32_e64 v10, v10, v14, s[2:3]
	v_cndmask_b32_e64 v11, v11, 4, s[2:3]
	v_cmp_gt_f32_e64 s[2:3], v15, v10
	s_nop 1
	v_cndmask_b32_e64 v10, v10, v15, s[2:3]
	v_cndmask_b32_e64 v11, v11, 5, s[2:3]
	v_cmp_gt_f32_e64 s[2:3], v16, v10
	s_nop 1
	v_cndmask_b32_e64 v10, v10, v16, s[2:3]
	v_cndmask_b32_e64 v11, v11, 6, s[2:3]
	v_cmp_gt_f32_e64 s[2:3], v17, v10
	s_nop 1
	v_cndmask_b32_e64 v10, v10, v17, s[2:3]
	v_cndmask_b32_e64 v11, v11, 7, s[2:3]
	s_waitcnt lgkmcnt(1)
	v_cmp_gt_f32_e64 s[2:3], v6, v10
	s_nop 1
	v_cndmask_b32_e64 v10, v10, v6, s[2:3]
	v_cndmask_b32_e64 v11, v11, 8, s[2:3]
	v_cmp_gt_f32_e64 s[2:3], v7, v10
	s_nop 1
	v_cndmask_b32_e64 v10, v10, v7, s[2:3]
	v_cndmask_b32_e64 v11, v11, 9, s[2:3]
	v_cmp_gt_f32_e64 s[2:3], v8, v10
	s_nop 1
	v_cndmask_b32_e64 v10, v10, v8, s[2:3]
	v_cndmask_b32_e64 v11, v11, 10, s[2:3]
	v_cmp_gt_f32_e64 s[2:3], v9, v10
	s_nop 1
	v_cndmask_b32_e64 v10, v10, v9, s[2:3]
	v_cndmask_b32_e64 v11, v11, 11, s[2:3]
	s_waitcnt lgkmcnt(0)
	v_cmp_gt_f32_e64 s[2:3], v2, v10
	s_nop 1
	v_cndmask_b32_e64 v10, v10, v2, s[2:3]
	v_cndmask_b32_e64 v11, v11, 12, s[2:3]
	v_cmp_gt_f32_e64 s[2:3], v3, v10
	s_nop 1
	v_cndmask_b32_e64 v10, v10, v3, s[2:3]
	v_cndmask_b32_e64 v11, v11, 13, s[2:3]
	v_cmp_gt_f32_e64 s[2:3], v4, v10
	s_nop 1
	v_cndmask_b32_e64 v10, v10, v4, s[2:3]
	v_cndmask_b32_e64 v11, v11, 14, s[2:3]
	v_cmp_gt_f32_e64 s[2:3], v5, v10
	s_nop 1
	v_cndmask_b32_e64 v18, v10, v5, s[2:3]
	v_cndmask_b32_e64 v19, v11, 15, s[2:3]
	ds_read_b128 v[10:13], v30 offset:64
	s_waitcnt lgkmcnt(0)
	v_cmp_gt_f32_e64 s[2:3], v10, v18
	s_nop 1
	v_cndmask_b32_e64 v18, v18, v10, s[2:3]
	v_cndmask_b32_e64 v19, v19, 16, s[2:3]
	v_cmp_gt_f32_e64 s[2:3], v11, v18
	s_nop 1
	v_cndmask_b32_e64 v18, v18, v11, s[2:3]
	v_cndmask_b32_e64 v19, v19, 17, s[2:3]
	v_cmp_gt_f32_e64 s[2:3], v12, v18
	s_nop 1
	v_cndmask_b32_e64 v18, v18, v12, s[2:3]
	v_cndmask_b32_e64 v19, v19, 18, s[2:3]
	v_cmp_gt_f32_e64 s[2:3], v13, v18
	s_nop 1
	v_cndmask_b32_e64 v26, v18, v13, s[2:3]
	v_cndmask_b32_e64 v27, v19, 19, s[2:3]
	ds_read_b128 v[18:21], v30 offset:80
	s_waitcnt lgkmcnt(0)
	v_cmp_gt_f32_e64 s[2:3], v18, v26
	s_nop 1
	v_cndmask_b32_e64 v26, v26, v18, s[2:3]
	v_cndmask_b32_e64 v27, v27, 20, s[2:3]
	v_cmp_gt_f32_e64 s[2:3], v19, v26
	s_nop 1
	v_cndmask_b32_e64 v26, v26, v19, s[2:3]
	v_cndmask_b32_e64 v27, v27, 21, s[2:3]
	v_cmp_gt_f32_e64 s[2:3], v20, v26
	s_nop 1
	v_cndmask_b32_e64 v26, v26, v20, s[2:3]
	v_cndmask_b32_e64 v27, v27, 22, s[2:3]
	v_cmp_gt_f32_e64 s[2:3], v21, v26
	s_nop 1
	v_cndmask_b32_e64 v31, v26, v21, s[2:3]
	v_cndmask_b32_e64 v32, v27, 23, s[2:3]
	ds_read_b128 v[26:29], v30 offset:96
	s_waitcnt lgkmcnt(0)
	v_cmp_gt_f32_e64 s[2:3], v26, v31
	s_nop 1
	v_cndmask_b32_e64 v31, v31, v26, s[2:3]
	v_cndmask_b32_e64 v32, v32, 24, s[2:3]
	v_cmp_gt_f32_e64 s[2:3], v27, v31
	s_nop 1
	v_cndmask_b32_e64 v31, v31, v27, s[2:3]
	v_cndmask_b32_e64 v32, v32, 25, s[2:3]
	v_cmp_gt_f32_e64 s[2:3], v28, v31
	s_nop 1
	v_cndmask_b32_e64 v31, v31, v28, s[2:3]
	v_cndmask_b32_e64 v32, v32, 26, s[2:3]
	v_cmp_gt_f32_e64 s[2:3], v29, v31
	s_nop 1
	v_cndmask_b32_e64 v38, v31, v29, s[2:3]
	v_cndmask_b32_e64 v39, v32, 27, s[2:3]
	ds_read_b128 v[30:33], v30 offset:112
	s_waitcnt lgkmcnt(0)
	v_cmp_gt_f32_e64 s[2:3], v30, v38
	s_nop 1
	v_cndmask_b32_e64 v38, v38, v30, s[2:3]
	v_cndmask_b32_e64 v39, v39, 28, s[2:3]
	v_cmp_gt_f32_e64 s[2:3], v31, v38
	s_nop 1
	v_cndmask_b32_e64 v38, v38, v31, s[2:3]
	v_cndmask_b32_e64 v39, v39, 29, s[2:3]
	v_cmp_gt_f32_e64 s[2:3], v32, v38
	s_nop 1
	v_cndmask_b32_e64 v38, v38, v32, s[2:3]
	v_cndmask_b32_e64 v40, v39, 30, s[2:3]
	v_cmp_gt_f32_e64 s[2:3], v33, v38
	s_nop 1
	v_cndmask_b32_e64 v39, v38, v33, s[2:3]
	v_cndmask_b32_e64 v38, v40, 31, s[2:3]
	v_cmp_ne_u32_e64 s[2:3], 0, v38
	v_lshlrev_b32_e64 v41, v38, 1
	s_and_b64 s[2:3], s[2:3], vcc
	v_cndmask_b32_e64 v40, v48, v22, s[2:3]
	v_and_b32_e32 v42, 2, v41
	v_cmp_eq_u32_e64 s[2:3], 0, v42
	v_cmp_gt_f32_e64 s[36:37], v23, v40
	s_and_b64 s[2:3], s[2:3], s[36:37]
	v_cndmask_b32_e64 v40, v40, v23, s[2:3]
	v_and_b32_e32 v43, 4, v41
	v_cndmask_b32_e64 v42, 0, 1, s[2:3]
	v_cmp_eq_u32_e64 s[2:3], 0, v43
	v_cmp_gt_f32_e64 s[36:37], v24, v40
	s_and_b64 s[2:3], s[2:3], s[36:37]
	v_cndmask_b32_e64 v40, v40, v24, s[2:3]
	v_and_b32_e32 v43, 8, v41
	v_cndmask_b32_e64 v42, v42, 2, s[2:3]
	v_cmp_eq_u32_e64 s[2:3], 0, v43
	v_cmp_gt_f32_e64 s[36:37], v25, v40
	s_and_b64 s[2:3], s[2:3], s[36:37]
	v_cndmask_b32_e64 v40, v40, v25, s[2:3]
	v_and_b32_e32 v43, 16, v41
	v_cndmask_b32_e64 v42, v42, 3, s[2:3]
	v_cmp_eq_u32_e64 s[2:3], 0, v43
	v_cmp_gt_f32_e64 s[36:37], v14, v40
	s_and_b64 s[2:3], s[2:3], s[36:37]
	v_cndmask_b32_e64 v40, v40, v14, s[2:3]
	v_and_b32_e32 v43, 32, v41
	v_cndmask_b32_e64 v42, v42, 4, s[2:3]
	v_cmp_eq_u32_e64 s[2:3], 0, v43
	v_cmp_gt_f32_e64 s[36:37], v15, v40
	s_and_b64 s[2:3], s[2:3], s[36:37]
	v_cndmask_b32_e64 v40, v40, v15, s[2:3]
	v_and_b32_e32 v43, 64, v41
	v_cndmask_b32_e64 v42, v42, 5, s[2:3]
	v_cmp_eq_u32_e64 s[2:3], 0, v43
	v_cmp_gt_f32_e64 s[36:37], v16, v40
	s_and_b64 s[2:3], s[2:3], s[36:37]
	v_cndmask_b32_e64 v40, v40, v16, s[2:3]
	v_and_b32_e32 v43, 0x80, v41
	v_cndmask_b32_e64 v42, v42, 6, s[2:3]
	v_cmp_eq_u32_e64 s[2:3], 0, v43
	v_cmp_gt_f32_e64 s[36:37], v17, v40
	s_and_b64 s[2:3], s[2:3], s[36:37]
	v_cndmask_b32_e64 v40, v40, v17, s[2:3]
	v_and_b32_e32 v43, 0x100, v41
	v_cndmask_b32_e64 v42, v42, 7, s[2:3]
	v_cmp_eq_u32_e64 s[2:3], 0, v43
	v_cmp_gt_f32_e64 s[36:37], v6, v40
	s_and_b64 s[2:3], s[2:3], s[36:37]
	v_cndmask_b32_e64 v40, v40, v6, s[2:3]
	v_and_b32_e32 v43, 0x200, v41
	v_cndmask_b32_e64 v42, v42, 8, s[2:3]
	v_cmp_eq_u32_e64 s[2:3], 0, v43
	v_cmp_gt_f32_e64 s[36:37], v7, v40
	s_and_b64 s[2:3], s[2:3], s[36:37]
	v_cndmask_b32_e64 v40, v40, v7, s[2:3]
	v_and_b32_e32 v43, 0x400, v41
	v_cndmask_b32_e64 v42, v42, 9, s[2:3]
	v_cmp_eq_u32_e64 s[2:3], 0, v43
	v_cmp_gt_f32_e64 s[36:37], v8, v40
	s_and_b64 s[2:3], s[2:3], s[36:37]
	v_cndmask_b32_e64 v40, v40, v8, s[2:3]
	v_and_b32_e32 v43, 0x800, v41
	v_cndmask_b32_e64 v42, v42, 10, s[2:3]
	v_cmp_eq_u32_e64 s[2:3], 0, v43
	v_cmp_gt_f32_e64 s[36:37], v9, v40
	s_and_b64 s[2:3], s[2:3], s[36:37]
	v_cndmask_b32_e64 v40, v40, v9, s[2:3]
	v_and_b32_e32 v43, 0x1000, v41
	v_cndmask_b32_e64 v42, v42, 11, s[2:3]
	v_cmp_eq_u32_e64 s[2:3], 0, v43
	v_cmp_gt_f32_e64 s[36:37], v2, v40
	s_and_b64 s[2:3], s[2:3], s[36:37]
	v_cndmask_b32_e64 v40, v40, v2, s[2:3]
	v_and_b32_e32 v43, 0x2000, v41
	v_cndmask_b32_e64 v42, v42, 12, s[2:3]
	v_cmp_eq_u32_e64 s[2:3], 0, v43
	v_cmp_gt_f32_e64 s[36:37], v3, v40
	s_and_b64 s[2:3], s[2:3], s[36:37]
	v_cndmask_b32_e64 v40, v40, v3, s[2:3]
	v_and_b32_e32 v43, 0x4000, v41
	v_cndmask_b32_e64 v42, v42, 13, s[2:3]
	v_cmp_eq_u32_e64 s[2:3], 0, v43
	v_cmp_gt_f32_e64 s[36:37], v4, v40
	s_and_b64 s[2:3], s[2:3], s[36:37]
	v_cndmask_b32_e64 v40, v40, v4, s[2:3]
	v_and_b32_e32 v43, 0x8000, v41
	v_cndmask_b32_e64 v42, v42, 14, s[2:3]
	v_cmp_eq_u32_e64 s[2:3], 0, v43
	v_cmp_gt_f32_e64 s[36:37], v5, v40
	s_and_b64 s[2:3], s[2:3], s[36:37]
	v_cndmask_b32_e64 v40, v40, v5, s[2:3]
	v_and_b32_e32 v43, 0x10000, v41
	v_cndmask_b32_e64 v42, v42, 15, s[2:3]
	v_cmp_eq_u32_e64 s[2:3], 0, v43
	v_cmp_gt_f32_e64 s[36:37], v10, v40
	s_and_b64 s[2:3], s[2:3], s[36:37]
	v_cndmask_b32_e64 v40, v40, v10, s[2:3]
	v_and_b32_e32 v43, 0x20000, v41
	v_cndmask_b32_e64 v42, v42, 16, s[2:3]
	v_cmp_eq_u32_e64 s[2:3], 0, v43
	v_cmp_gt_f32_e64 s[36:37], v11, v40
	s_and_b64 s[2:3], s[2:3], s[36:37]
	v_cndmask_b32_e64 v40, v40, v11, s[2:3]
	v_and_b32_e32 v43, 0x40000, v41
	v_cndmask_b32_e64 v42, v42, 17, s[2:3]
	v_cmp_eq_u32_e64 s[2:3], 0, v43
	v_cmp_gt_f32_e64 s[36:37], v12, v40
	s_and_b64 s[2:3], s[2:3], s[36:37]
	v_cndmask_b32_e64 v40, v40, v12, s[2:3]
	v_and_b32_e32 v43, 0x80000, v41
	v_cndmask_b32_e64 v42, v42, 18, s[2:3]
	v_cmp_eq_u32_e64 s[2:3], 0, v43
	v_cmp_gt_f32_e64 s[36:37], v13, v40
	s_and_b64 s[2:3], s[2:3], s[36:37]
	v_cndmask_b32_e64 v40, v40, v13, s[2:3]
	v_and_b32_e32 v43, 0x100000, v41
	v_cndmask_b32_e64 v42, v42, 19, s[2:3]
	v_cmp_eq_u32_e64 s[2:3], 0, v43
	v_cmp_gt_f32_e64 s[36:37], v18, v40
	s_and_b64 s[2:3], s[2:3], s[36:37]
	v_cndmask_b32_e64 v40, v40, v18, s[2:3]
	v_and_b32_e32 v43, 0x200000, v41
	v_cndmask_b32_e64 v42, v42, 20, s[2:3]
	v_cmp_eq_u32_e64 s[2:3], 0, v43
	v_cmp_gt_f32_e64 s[36:37], v19, v40
	s_and_b64 s[2:3], s[2:3], s[36:37]
	v_cndmask_b32_e64 v40, v40, v19, s[2:3]
	v_and_b32_e32 v43, 0x400000, v41
	v_cndmask_b32_e64 v42, v42, 21, s[2:3]
	v_cmp_eq_u32_e64 s[2:3], 0, v43
	v_cmp_gt_f32_e64 s[36:37], v20, v40
	s_and_b64 s[2:3], s[2:3], s[36:37]
	v_cndmask_b32_e64 v40, v40, v20, s[2:3]
	v_and_b32_e32 v43, 0x800000, v41
	v_cndmask_b32_e64 v42, v42, 22, s[2:3]
	v_cmp_eq_u32_e64 s[2:3], 0, v43
	v_cmp_gt_f32_e64 s[36:37], v21, v40
	s_and_b64 s[2:3], s[2:3], s[36:37]
	v_cndmask_b32_e64 v40, v40, v21, s[2:3]
	v_and_b32_e32 v43, 0x1000000, v41
	v_cndmask_b32_e64 v42, v42, 23, s[2:3]
	v_cmp_eq_u32_e64 s[2:3], 0, v43
	v_cmp_gt_f32_e64 s[36:37], v26, v40
	s_and_b64 s[2:3], s[2:3], s[36:37]
	v_cndmask_b32_e64 v40, v40, v26, s[2:3]
	v_and_b32_e32 v43, 0x2000000, v41
	v_cndmask_b32_e64 v42, v42, 24, s[2:3]
	v_cmp_eq_u32_e64 s[2:3], 0, v43
	v_cmp_gt_f32_e64 s[36:37], v27, v40
	s_and_b64 s[2:3], s[2:3], s[36:37]
	v_cndmask_b32_e64 v40, v40, v27, s[2:3]
	v_and_b32_e32 v43, 0x4000000, v41
	v_cndmask_b32_e64 v42, v42, 25, s[2:3]
	v_cmp_eq_u32_e64 s[2:3], 0, v43
	v_cmp_gt_f32_e64 s[36:37], v28, v40
	s_and_b64 s[2:3], s[2:3], s[36:37]
	v_cndmask_b32_e64 v40, v40, v28, s[2:3]
	v_and_b32_e32 v43, 0x8000000, v41
	v_cndmask_b32_e64 v42, v42, 26, s[2:3]
	v_cmp_eq_u32_e64 s[2:3], 0, v43
	v_cmp_gt_f32_e64 s[36:37], v29, v40
	s_and_b64 s[2:3], s[2:3], s[36:37]
	v_cndmask_b32_e64 v40, v40, v29, s[2:3]
	v_and_b32_e32 v43, 0x10000000, v41
	v_cndmask_b32_e64 v42, v42, 27, s[2:3]
	v_cmp_eq_u32_e64 s[2:3], 0, v43
	v_cmp_gt_f32_e64 s[36:37], v30, v40
	s_and_b64 s[2:3], s[2:3], s[36:37]
	v_cndmask_b32_e64 v40, v40, v30, s[2:3]
	v_and_b32_e32 v43, 0x20000000, v41
	v_cndmask_b32_e64 v42, v42, 28, s[2:3]
	v_cmp_eq_u32_e64 s[2:3], 0, v43
	v_cmp_gt_f32_e64 s[36:37], v31, v40
	s_and_b64 s[2:3], s[2:3], s[36:37]
	v_cndmask_b32_e64 v40, v40, v31, s[2:3]
	v_and_b32_e32 v43, 2.0, v41
	v_cndmask_b32_e64 v42, v42, 29, s[2:3]
	v_cmp_eq_u32_e64 s[2:3], 0, v43
	v_cmp_gt_f32_e64 s[36:37], v32, v40
	s_and_b64 s[2:3], s[2:3], s[36:37]
	v_cndmask_b32_e64 v40, v40, v32, s[2:3]
	v_cndmask_b32_e64 v42, v42, 30, s[2:3]
	v_cmp_ne_u32_e64 s[2:3], 31, v38
	v_cmp_gt_f32_e64 s[36:37], v33, v40
	s_and_b64 s[2:3], s[2:3], s[36:37]
	v_cndmask_b32_e64 v43, v40, v33, s[2:3]
	v_cndmask_b32_e64 v40, v42, 31, s[2:3]
	v_lshl_or_b32 v41, 1, v40, v41
	v_and_b32_e32 v42, 1, v41
	v_cmp_eq_u32_e64 s[2:3], 0, v42
	s_and_b64 s[2:3], s[2:3], vcc
	v_and_b32_e32 v44, 2, v41
	v_cndmask_b32_e64 v42, v48, v22, s[2:3]
	v_cmp_eq_u32_e64 s[2:3], 0, v44
	v_cmp_gt_f32_e64 s[36:37], v23, v42
	s_and_b64 s[2:3], s[2:3], s[36:37]
	v_cndmask_b32_e64 v42, v42, v23, s[2:3]
	v_and_b32_e32 v45, 4, v41
	v_cndmask_b32_e64 v44, 0, 1, s[2:3]
	v_cmp_eq_u32_e64 s[2:3], 0, v45
	v_cmp_gt_f32_e64 s[36:37], v24, v42
	s_and_b64 s[2:3], s[2:3], s[36:37]
	v_cndmask_b32_e64 v42, v42, v24, s[2:3]
	v_and_b32_e32 v45, 8, v41
	v_cndmask_b32_e64 v44, v44, 2, s[2:3]
	v_cmp_eq_u32_e64 s[2:3], 0, v45
	v_cmp_gt_f32_e64 s[36:37], v25, v42
	s_and_b64 s[2:3], s[2:3], s[36:37]
	v_cndmask_b32_e64 v42, v42, v25, s[2:3]
	v_and_b32_e32 v45, 16, v41
	v_cndmask_b32_e64 v44, v44, 3, s[2:3]
	v_cmp_eq_u32_e64 s[2:3], 0, v45
	v_cmp_gt_f32_e64 s[36:37], v14, v42
	s_and_b64 s[2:3], s[2:3], s[36:37]
	v_cndmask_b32_e64 v42, v42, v14, s[2:3]
	v_and_b32_e32 v45, 32, v41
	v_cndmask_b32_e64 v44, v44, 4, s[2:3]
	v_cmp_eq_u32_e64 s[2:3], 0, v45
	v_cmp_gt_f32_e64 s[36:37], v15, v42
	s_and_b64 s[2:3], s[2:3], s[36:37]
	v_cndmask_b32_e64 v42, v42, v15, s[2:3]
	v_and_b32_e32 v45, 64, v41
	v_cndmask_b32_e64 v44, v44, 5, s[2:3]
	v_cmp_eq_u32_e64 s[2:3], 0, v45
	v_cmp_gt_f32_e64 s[36:37], v16, v42
	s_and_b64 s[2:3], s[2:3], s[36:37]
	v_cndmask_b32_e64 v42, v42, v16, s[2:3]
	v_and_b32_e32 v45, 0x80, v41
	v_cndmask_b32_e64 v44, v44, 6, s[2:3]
	v_cmp_eq_u32_e64 s[2:3], 0, v45
	v_cmp_gt_f32_e64 s[36:37], v17, v42
	s_and_b64 s[2:3], s[2:3], s[36:37]
	v_cndmask_b32_e64 v42, v42, v17, s[2:3]
	v_and_b32_e32 v45, 0x100, v41
	v_cndmask_b32_e64 v44, v44, 7, s[2:3]
	v_cmp_eq_u32_e64 s[2:3], 0, v45
	v_cmp_gt_f32_e64 s[36:37], v6, v42
	s_and_b64 s[2:3], s[2:3], s[36:37]
	v_cndmask_b32_e64 v42, v42, v6, s[2:3]
	v_and_b32_e32 v45, 0x200, v41
	v_cndmask_b32_e64 v44, v44, 8, s[2:3]
	v_cmp_eq_u32_e64 s[2:3], 0, v45
	v_cmp_gt_f32_e64 s[36:37], v7, v42
	s_and_b64 s[2:3], s[2:3], s[36:37]
	v_cndmask_b32_e64 v42, v42, v7, s[2:3]
	v_and_b32_e32 v45, 0x400, v41
	v_cndmask_b32_e64 v44, v44, 9, s[2:3]
	v_cmp_eq_u32_e64 s[2:3], 0, v45
	v_cmp_gt_f32_e64 s[36:37], v8, v42
	s_and_b64 s[2:3], s[2:3], s[36:37]
	v_cndmask_b32_e64 v42, v42, v8, s[2:3]
	v_and_b32_e32 v45, 0x800, v41
	v_cndmask_b32_e64 v44, v44, 10, s[2:3]
	v_cmp_eq_u32_e64 s[2:3], 0, v45
	v_cmp_gt_f32_e64 s[36:37], v9, v42
	s_and_b64 s[2:3], s[2:3], s[36:37]
	v_cndmask_b32_e64 v42, v42, v9, s[2:3]
	v_and_b32_e32 v45, 0x1000, v41
	v_cndmask_b32_e64 v44, v44, 11, s[2:3]
	v_cmp_eq_u32_e64 s[2:3], 0, v45
	v_cmp_gt_f32_e64 s[36:37], v2, v42
	s_and_b64 s[2:3], s[2:3], s[36:37]
	v_cndmask_b32_e64 v42, v42, v2, s[2:3]
	v_and_b32_e32 v45, 0x2000, v41
	v_cndmask_b32_e64 v44, v44, 12, s[2:3]
	v_cmp_eq_u32_e64 s[2:3], 0, v45
	v_cmp_gt_f32_e64 s[36:37], v3, v42
	s_and_b64 s[2:3], s[2:3], s[36:37]
	v_cndmask_b32_e64 v42, v42, v3, s[2:3]
	v_and_b32_e32 v45, 0x4000, v41
	v_cndmask_b32_e64 v44, v44, 13, s[2:3]
	v_cmp_eq_u32_e64 s[2:3], 0, v45
	v_cmp_gt_f32_e64 s[36:37], v4, v42
	s_and_b64 s[2:3], s[2:3], s[36:37]
	v_cndmask_b32_e64 v42, v42, v4, s[2:3]
	v_and_b32_e32 v45, 0x8000, v41
	v_cndmask_b32_e64 v44, v44, 14, s[2:3]
	v_cmp_eq_u32_e64 s[2:3], 0, v45
	v_cmp_gt_f32_e64 s[36:37], v5, v42
	s_and_b64 s[2:3], s[2:3], s[36:37]
	v_cndmask_b32_e64 v42, v42, v5, s[2:3]
	v_and_b32_e32 v45, 0x10000, v41
	v_cndmask_b32_e64 v44, v44, 15, s[2:3]
	v_cmp_eq_u32_e64 s[2:3], 0, v45
	v_cmp_gt_f32_e64 s[36:37], v10, v42
	s_and_b64 s[2:3], s[2:3], s[36:37]
	v_cndmask_b32_e64 v42, v42, v10, s[2:3]
	v_and_b32_e32 v45, 0x20000, v41
	v_cndmask_b32_e64 v44, v44, 16, s[2:3]
	v_cmp_eq_u32_e64 s[2:3], 0, v45
	v_cmp_gt_f32_e64 s[36:37], v11, v42
	s_and_b64 s[2:3], s[2:3], s[36:37]
	v_cndmask_b32_e64 v42, v42, v11, s[2:3]
	v_and_b32_e32 v45, 0x40000, v41
	v_cndmask_b32_e64 v44, v44, 17, s[2:3]
	v_cmp_eq_u32_e64 s[2:3], 0, v45
	v_cmp_gt_f32_e64 s[36:37], v12, v42
	s_and_b64 s[2:3], s[2:3], s[36:37]
	v_cndmask_b32_e64 v42, v42, v12, s[2:3]
	v_and_b32_e32 v45, 0x80000, v41
	v_cndmask_b32_e64 v44, v44, 18, s[2:3]
	v_cmp_eq_u32_e64 s[2:3], 0, v45
	v_cmp_gt_f32_e64 s[36:37], v13, v42
	s_and_b64 s[2:3], s[2:3], s[36:37]
	v_cndmask_b32_e64 v42, v42, v13, s[2:3]
	v_and_b32_e32 v45, 0x100000, v41
	v_cndmask_b32_e64 v44, v44, 19, s[2:3]
	v_cmp_eq_u32_e64 s[2:3], 0, v45
	v_cmp_gt_f32_e64 s[36:37], v18, v42
	s_and_b64 s[2:3], s[2:3], s[36:37]
	v_cndmask_b32_e64 v42, v42, v18, s[2:3]
	v_and_b32_e32 v45, 0x200000, v41
	v_cndmask_b32_e64 v44, v44, 20, s[2:3]
	v_cmp_eq_u32_e64 s[2:3], 0, v45
	v_cmp_gt_f32_e64 s[36:37], v19, v42
	s_and_b64 s[2:3], s[2:3], s[36:37]
	v_cndmask_b32_e64 v42, v42, v19, s[2:3]
	v_and_b32_e32 v45, 0x400000, v41
	v_cndmask_b32_e64 v44, v44, 21, s[2:3]
	v_cmp_eq_u32_e64 s[2:3], 0, v45
	v_cmp_gt_f32_e64 s[36:37], v20, v42
	s_and_b64 s[2:3], s[2:3], s[36:37]
	v_cndmask_b32_e64 v42, v42, v20, s[2:3]
	v_and_b32_e32 v45, 0x800000, v41
	v_cndmask_b32_e64 v44, v44, 22, s[2:3]
	v_cmp_eq_u32_e64 s[2:3], 0, v45
	v_cmp_gt_f32_e64 s[36:37], v21, v42
	s_and_b64 s[2:3], s[2:3], s[36:37]
	v_cndmask_b32_e64 v42, v42, v21, s[2:3]
	v_and_b32_e32 v45, 0x1000000, v41
	v_cndmask_b32_e64 v44, v44, 23, s[2:3]
	v_cmp_eq_u32_e64 s[2:3], 0, v45
	v_cmp_gt_f32_e64 s[36:37], v26, v42
	s_and_b64 s[2:3], s[2:3], s[36:37]
	v_cndmask_b32_e64 v42, v42, v26, s[2:3]
	v_and_b32_e32 v45, 0x2000000, v41
	v_cndmask_b32_e64 v44, v44, 24, s[2:3]
	v_cmp_eq_u32_e64 s[2:3], 0, v45
	v_cmp_gt_f32_e64 s[36:37], v27, v42
	s_and_b64 s[2:3], s[2:3], s[36:37]
	v_cndmask_b32_e64 v42, v42, v27, s[2:3]
	v_and_b32_e32 v45, 0x4000000, v41
	v_cndmask_b32_e64 v44, v44, 25, s[2:3]
	v_cmp_eq_u32_e64 s[2:3], 0, v45
	v_cmp_gt_f32_e64 s[36:37], v28, v42
	s_and_b64 s[2:3], s[2:3], s[36:37]
	v_cndmask_b32_e64 v42, v42, v28, s[2:3]
	v_and_b32_e32 v45, 0x8000000, v41
	v_cndmask_b32_e64 v44, v44, 26, s[2:3]
	v_cmp_eq_u32_e64 s[2:3], 0, v45
	v_cmp_gt_f32_e64 s[36:37], v29, v42
	s_and_b64 s[2:3], s[2:3], s[36:37]
	v_cndmask_b32_e64 v42, v42, v29, s[2:3]
	v_and_b32_e32 v45, 0x10000000, v41
	v_cndmask_b32_e64 v44, v44, 27, s[2:3]
	v_cmp_eq_u32_e64 s[2:3], 0, v45
	v_cmp_gt_f32_e64 s[36:37], v30, v42
	s_and_b64 s[2:3], s[2:3], s[36:37]
	v_cndmask_b32_e64 v42, v42, v30, s[2:3]
	v_and_b32_e32 v45, 0x20000000, v41
	v_cndmask_b32_e64 v44, v44, 28, s[2:3]
	v_cmp_eq_u32_e64 s[2:3], 0, v45
	v_cmp_gt_f32_e64 s[36:37], v31, v42
	s_and_b64 s[2:3], s[2:3], s[36:37]
	v_cndmask_b32_e64 v42, v42, v31, s[2:3]
	v_and_b32_e32 v45, 2.0, v41
	v_cndmask_b32_e64 v44, v44, 29, s[2:3]
	v_cmp_eq_u32_e64 s[2:3], 0, v45
	v_cmp_gt_f32_e64 s[36:37], v32, v42
	s_and_b64 s[2:3], s[2:3], s[36:37]
	v_cndmask_b32_e64 v42, v42, v32, s[2:3]
	v_cndmask_b32_e64 v44, v44, 30, s[2:3]
	v_cmp_lt_i32_e64 s[2:3], -1, v41
	v_cmp_gt_f32_e64 s[36:37], v33, v42
	s_and_b64 s[2:3], s[2:3], s[36:37]
	v_cndmask_b32_e64 v44, v44, 31, s[2:3]
	v_lshlrev_b32_e64 v45, v44, 1
	v_bitop3_b32 v47, v45, 1, v41 bitop3:0xc8
	v_cndmask_b32_e64 v42, v42, v33, s[2:3]
	v_cmp_eq_u32_e64 s[2:3], 0, v47
	s_and_b64 vcc, s[2:3], vcc
	v_cndmask_b32_e32 v22, v48, v22, vcc
	v_bitop3_b32 v47, v45, 2, v41 bitop3:0xc8
	v_cmp_eq_u32_e32 vcc, 0, v47
	v_cmp_gt_f32_e64 s[2:3], v23, v22
	s_and_b64 vcc, vcc, s[2:3]
	v_cndmask_b32_e32 v22, v22, v23, vcc
	v_bitop3_b32 v47, v45, 4, v41 bitop3:0xc8
	v_cndmask_b32_e64 v23, 0, 1, vcc
	v_cmp_eq_u32_e32 vcc, 0, v47
	v_cmp_gt_f32_e64 s[2:3], v24, v22
	s_and_b64 vcc, vcc, s[2:3]
	v_cndmask_b32_e32 v22, v22, v24, vcc
	v_bitop3_b32 v24, v45, 8, v41 bitop3:0xc8
	v_cndmask_b32_e64 v23, v23, 2, vcc
	v_cmp_eq_u32_e32 vcc, 0, v24
	v_cmp_gt_f32_e64 s[2:3], v25, v22
	s_and_b64 vcc, vcc, s[2:3]
	v_cndmask_b32_e32 v22, v22, v25, vcc
	v_bitop3_b32 v24, v45, 16, v41 bitop3:0xc8
	v_cndmask_b32_e64 v23, v23, 3, vcc
	v_cmp_eq_u32_e32 vcc, 0, v24
	v_cmp_gt_f32_e64 s[2:3], v14, v22
	s_and_b64 vcc, vcc, s[2:3]
	v_cndmask_b32_e32 v14, v22, v14, vcc
	v_cndmask_b32_e64 v22, v23, 4, vcc
	v_bitop3_b32 v23, v45, 32, v41 bitop3:0xc8
	v_cmp_eq_u32_e32 vcc, 0, v23
	v_cmp_gt_f32_e64 s[2:3], v15, v14
	s_and_b64 vcc, vcc, s[2:3]
	v_cndmask_b32_e32 v14, v14, v15, vcc
	v_cndmask_b32_e64 v15, v22, 5, vcc
	v_bitop3_b32 v22, v45, 64, v41 bitop3:0xc8
	v_cmp_eq_u32_e32 vcc, 0, v22
	v_cmp_gt_f32_e64 s[2:3], v16, v14
	s_and_b64 vcc, vcc, s[2:3]
	s_movk_i32 s2, 0x80
	v_cndmask_b32_e32 v14, v14, v16, vcc
	v_bitop3_b32 v16, v45, s2, v41 bitop3:0xc8
	v_cndmask_b32_e64 v15, v15, 6, vcc
	v_cmp_eq_u32_e32 vcc, 0, v16
	v_cmp_gt_f32_e64 s[2:3], v17, v14
	s_and_b64 vcc, vcc, s[2:3]
	s_movk_i32 s2, 0x100
	v_cndmask_b32_e32 v14, v14, v17, vcc
	v_bitop3_b32 v16, v45, s2, v41 bitop3:0xc8
	v_cndmask_b32_e64 v15, v15, 7, vcc
	v_cmp_eq_u32_e32 vcc, 0, v16
	v_cmp_gt_f32_e64 s[2:3], v6, v14
	s_and_b64 vcc, vcc, s[2:3]
	s_movk_i32 s2, 0x200
	v_cndmask_b32_e32 v6, v14, v6, vcc
	v_cndmask_b32_e64 v14, v15, 8, vcc
	v_bitop3_b32 v15, v45, s2, v41 bitop3:0xc8
	v_cmp_eq_u32_e32 vcc, 0, v15
	v_cmp_gt_f32_e64 s[2:3], v7, v6
	s_and_b64 vcc, vcc, s[2:3]
	s_movk_i32 s2, 0x400
	v_cndmask_b32_e32 v6, v6, v7, vcc
	v_cndmask_b32_e64 v7, v14, 9, vcc
	v_bitop3_b32 v14, v45, s2, v41 bitop3:0xc8
	v_cmp_eq_u32_e32 vcc, 0, v14
	v_cmp_gt_f32_e64 s[2:3], v8, v6
	s_and_b64 vcc, vcc, s[2:3]
	s_movk_i32 s2, 0x800
	v_cndmask_b32_e32 v6, v6, v8, vcc
	v_bitop3_b32 v8, v45, s2, v41 bitop3:0xc8
	v_cndmask_b32_e64 v7, v7, 10, vcc
	v_cmp_eq_u32_e32 vcc, 0, v8
	v_cmp_gt_f32_e64 s[2:3], v9, v6
	s_and_b64 vcc, vcc, s[2:3]
	s_movk_i32 s2, 0x1000
	v_cndmask_b32_e32 v6, v6, v9, vcc
	v_bitop3_b32 v8, v45, s2, v41 bitop3:0xc8
	v_cndmask_b32_e64 v7, v7, 11, vcc
	v_cmp_eq_u32_e32 vcc, 0, v8
	v_cmp_gt_f32_e64 s[2:3], v2, v6
	s_and_b64 vcc, vcc, s[2:3]
	s_movk_i32 s2, 0x2000
	v_cndmask_b32_e32 v2, v6, v2, vcc
	v_cndmask_b32_e64 v6, v7, 12, vcc
	v_bitop3_b32 v7, v45, s2, v41 bitop3:0xc8
	v_cmp_eq_u32_e32 vcc, 0, v7
	v_cmp_gt_f32_e64 s[2:3], v3, v2
	s_and_b64 vcc, vcc, s[2:3]
	s_movk_i32 s2, 0x4000
	v_cndmask_b32_e32 v2, v2, v3, vcc
	v_cndmask_b32_e64 v3, v6, 13, vcc
	v_bitop3_b32 v6, v45, s2, v41 bitop3:0xc8
	v_cmp_eq_u32_e32 vcc, 0, v6
	v_cmp_gt_f32_e64 s[2:3], v4, v2
	s_and_b64 vcc, vcc, s[2:3]
	s_mov_b32 s2, 0x8000
	v_cndmask_b32_e32 v2, v2, v4, vcc
	v_bitop3_b32 v4, v45, s2, v41 bitop3:0xc8
	v_cndmask_b32_e64 v3, v3, 14, vcc
	v_cmp_eq_u32_e32 vcc, 0, v4
	v_cmp_gt_f32_e64 s[2:3], v5, v2
	s_and_b64 vcc, vcc, s[2:3]
	s_mov_b32 s2, 0x10000
	v_cndmask_b32_e32 v2, v2, v5, vcc
	v_bitop3_b32 v4, v45, s2, v41 bitop3:0xc8
	v_cndmask_b32_e64 v3, v3, 15, vcc
	v_cmp_eq_u32_e32 vcc, 0, v4
	v_cmp_gt_f32_e64 s[2:3], v10, v2
	s_and_b64 vcc, vcc, s[2:3]
	s_mov_b32 s2, 0x20000
	v_cndmask_b32_e32 v2, v2, v10, vcc
	v_bitop3_b32 v4, v45, s2, v41 bitop3:0xc8
	v_cndmask_b32_e64 v3, v3, 16, vcc
	v_cmp_eq_u32_e32 vcc, 0, v4
	v_cmp_gt_f32_e64 s[2:3], v11, v2
	s_and_b64 vcc, vcc, s[2:3]
	s_mov_b32 s2, 0x40000
	v_cndmask_b32_e32 v2, v2, v11, vcc
	v_bitop3_b32 v4, v45, s2, v41 bitop3:0xc8
	v_cndmask_b32_e64 v3, v3, 17, vcc
	v_cmp_eq_u32_e32 vcc, 0, v4
	v_cmp_gt_f32_e64 s[2:3], v12, v2
	s_and_b64 vcc, vcc, s[2:3]
	s_mov_b32 s2, 0x80000
	v_cndmask_b32_e32 v2, v2, v12, vcc
	v_bitop3_b32 v4, v45, s2, v41 bitop3:0xc8
	v_cndmask_b32_e64 v3, v3, 18, vcc
	v_cmp_eq_u32_e32 vcc, 0, v4
	v_cmp_gt_f32_e64 s[2:3], v13, v2
	s_and_b64 vcc, vcc, s[2:3]
	s_mov_b32 s2, 0x100000
	v_cndmask_b32_e32 v2, v2, v13, vcc
	v_bitop3_b32 v4, v45, s2, v41 bitop3:0xc8
	v_cndmask_b32_e64 v3, v3, 19, vcc
	v_cmp_eq_u32_e32 vcc, 0, v4
	v_cmp_gt_f32_e64 s[2:3], v18, v2
	s_and_b64 vcc, vcc, s[2:3]
	s_mov_b32 s2, 0x200000
	v_cndmask_b32_e32 v2, v2, v18, vcc
	v_bitop3_b32 v4, v45, s2, v41 bitop3:0xc8
	v_cndmask_b32_e64 v3, v3, 20, vcc
	v_cmp_eq_u32_e32 vcc, 0, v4
	v_cmp_gt_f32_e64 s[2:3], v19, v2
	s_and_b64 vcc, vcc, s[2:3]
	s_mov_b32 s2, 0x400000
	v_cndmask_b32_e32 v2, v2, v19, vcc
	v_bitop3_b32 v4, v45, s2, v41 bitop3:0xc8
	v_cndmask_b32_e64 v3, v3, 21, vcc
	v_cmp_eq_u32_e32 vcc, 0, v4
	v_cmp_gt_f32_e64 s[2:3], v20, v2
	s_and_b64 vcc, vcc, s[2:3]
	v_cndmask_b32_e32 v2, v2, v20, vcc
	v_bitop3_b32 v4, v45, s77, v41 bitop3:0xc8
	v_cndmask_b32_e64 v3, v3, 22, vcc
	v_cmp_eq_u32_e32 vcc, 0, v4
	v_cmp_gt_f32_e64 s[2:3], v21, v2
	s_and_b64 vcc, vcc, s[2:3]
	s_mov_b32 s2, 0x1000000
	v_cndmask_b32_e32 v2, v2, v21, vcc
	v_bitop3_b32 v4, v45, s2, v41 bitop3:0xc8
	v_cndmask_b32_e64 v3, v3, 23, vcc
	v_cmp_eq_u32_e32 vcc, 0, v4
	v_cmp_gt_f32_e64 s[2:3], v26, v2
	s_and_b64 vcc, vcc, s[2:3]
	s_brev_b32 s2, 64
	v_cndmask_b32_e32 v2, v2, v26, vcc
	v_bitop3_b32 v4, v45, s2, v41 bitop3:0xc8
	v_cndmask_b32_e64 v3, v3, 24, vcc
	v_cmp_eq_u32_e32 vcc, 0, v4
	v_cmp_gt_f32_e64 s[2:3], v27, v2
	s_and_b64 vcc, vcc, s[2:3]
	s_brev_b32 s2, 32
	v_cndmask_b32_e32 v2, v2, v27, vcc
	v_bitop3_b32 v4, v45, s2, v41 bitop3:0xc8
	v_cndmask_b32_e64 v3, v3, 25, vcc
	v_cmp_eq_u32_e32 vcc, 0, v4
	v_cmp_gt_f32_e64 s[2:3], v28, v2
	s_and_b64 vcc, vcc, s[2:3]
	s_brev_b32 s2, 16
	v_cndmask_b32_e32 v2, v2, v28, vcc
	v_bitop3_b32 v4, v45, s2, v41 bitop3:0xc8
	v_cndmask_b32_e64 v3, v3, 26, vcc
	v_cmp_eq_u32_e32 vcc, 0, v4
	v_cmp_gt_f32_e64 s[2:3], v29, v2
	s_and_b64 vcc, vcc, s[2:3]
	s_brev_b32 s2, 8
	v_cndmask_b32_e32 v2, v2, v29, vcc
	v_bitop3_b32 v4, v45, s2, v41 bitop3:0xc8
	v_cndmask_b32_e64 v3, v3, 27, vcc
	v_cmp_eq_u32_e32 vcc, 0, v4
	v_cmp_gt_f32_e64 s[2:3], v30, v2
	s_and_b64 vcc, vcc, s[2:3]
	s_brev_b32 s2, 4
	v_cndmask_b32_e32 v2, v2, v30, vcc
	v_bitop3_b32 v4, v45, s2, v41 bitop3:0xc8
	v_cndmask_b32_e64 v3, v3, 28, vcc
	v_cmp_eq_u32_e32 vcc, 0, v4
	v_cmp_gt_f32_e64 s[2:3], v31, v2
	s_and_b64 vcc, vcc, s[2:3]
	v_cndmask_b32_e32 v2, v2, v31, vcc
	v_bitop3_b32 v4, v45, 2.0, v41 bitop3:0xc8
	v_cndmask_b32_e64 v3, v3, 29, vcc
	v_cmp_eq_u32_e32 vcc, 0, v4
	v_cmp_gt_f32_e64 s[2:3], v32, v2
	s_and_b64 vcc, vcc, s[2:3]
	v_or_b32_e32 v46, v45, v41
	v_cndmask_b32_e32 v2, v2, v32, vcc
	v_cndmask_b32_e64 v3, v3, 30, vcc
	v_cmp_lt_i32_e32 vcc, -1, v46
	v_cmp_gt_f32_e64 s[2:3], v33, v2
	s_and_b64 vcc, vcc, s[2:3]
	v_cndmask_b32_e32 v5, v2, v33, vcc
	v_sub_f32_e32 v2, v39, v39
	v_cndmask_b32_e64 v7, v3, 31, vcc
	v_mul_f32_e32 v2, 0x3fb8aa3b, v2
	v_sub_f32_e32 v3, v43, v39
	v_exp_f32_e32 v2, v2
	v_mul_f32_e32 v3, 0x3fb8aa3b, v3
	v_exp_f32_e32 v3, v3
	v_sub_f32_e32 v5, v5, v39
	v_add_f32_e32 v4, 0, v2
	v_mul_f32_e32 v5, 0x3fb8aa3b, v5
	v_add_f32_e32 v6, v4, v3
	v_sub_f32_e32 v4, v42, v39
	v_mul_f32_e32 v4, 0x3fb8aa3b, v4
	v_exp_f32_e32 v4, v4
	v_exp_f32_e32 v5, v5
	v_add_f32_e32 v6, v6, v4
	v_add_f32_e32 v6, v6, v5
	v_div_scale_f32 v8, s[2:3], v6, v6, 1.0
	v_rcp_f32_e32 v9, v8
	s_add_i32 s2, 0, 0x23000
	v_fma_f32 v10, -v8, v9, 1.0
	v_fmac_f32_e32 v9, v10, v9
	v_div_scale_f32 v10, vcc, 1.0, v6, 1.0
	v_mul_f32_e32 v11, v10, v9
	v_fma_f32 v12, -v8, v11, v10
	v_fmac_f32_e32 v11, v12, v9
	v_fma_f32 v8, -v8, v11, v10
	v_div_fmas_f32 v8, v8, v9, v11
	v_div_fixup_f32 v6, v8, v6, 1.0
	v_or_b32_e32 v8, s12, v35
	v_lshlrev_b32_e32 v98, 2, v8
	v_lshl_add_u32 v8, v38, 2, s2
	ds_add_rtn_u32 v8, v8, v224
	v_lshlrev_b32_e32 v9, 17, v38
	v_add_u32_e32 v10, 0x22800, v37
	v_lshl_add_u32 v11, v40, 2, s2
	v_lshlrev_b32_e32 v12, 17, v40
	s_waitcnt lgkmcnt(0)
	v_lshlrev_b32_e32 v8, 22, v8
	v_or3_b32 v8, v8, v9, v98
	ds_write_b32 v10, v8
	ds_add_rtn_u32 v11, v11, v224
	v_pk_mul_f32 v[2:3], v[2:3], v[6:7] op_sel_hi:[1,0]
	v_lshl_add_u64 v[8:9], v[98:99], 2, s[8:9]
	s_waitcnt lgkmcnt(0)
	v_lshl_or_b32 v11, v11, 22, v12
	v_or3_b32 v11, v98, v11, 1
	ds_write_b32 v10, v11 offset:4
	v_lshl_add_u32 v11, v44, 2, s2
	ds_add_rtn_u32 v11, v11, v224
	v_lshlrev_b32_e32 v12, 17, v44
	s_waitcnt lgkmcnt(0)
	v_lshl_or_b32 v11, v11, 22, v12
	v_or3_b32 v11, v98, v11, 2
	ds_write_b32 v10, v11 offset:8
	v_lshl_add_u32 v11, v7, 2, s2
	ds_add_rtn_u32 v11, v11, v224
	v_lshlrev_b32_e32 v7, 17, v7
	s_waitcnt lgkmcnt(0)
	v_lshl_or_b32 v7, v11, 22, v7
	v_or3_b32 v7, v98, v7, 3
	v_pk_mul_f32 v[4:5], v[4:5], v[6:7] op_sel_hi:[1,0]
	v_add_co_u32_e32 v6, vcc, 0x49cba000, v8
	ds_write_b32 v10, v7 offset:12
	s_nop 0
	v_addc_co_u32_e32 v7, vcc, 0, v9, vcc
	global_store_dwordx4 v[6:7], v[2:5], off

.LBB0_2841:
	s_ashr_i32 s37, s19, 31
	s_mov_b32 s36, s19
	s_lshl_b64 s[36:37], s[36:37], 19
	s_add_u32 s36, s25, s36
	s_addc_u32 s37, s26, s37
	s_and_b64 s[40:41], s[40:41], exec
	s_cselect_b32 s31, s37, s39
	s_cselect_b32 s51, s36, s38
	v_mov_b32_e32 v61, v99
	v_mov_b32_e32 v65, v99
	s_add_u32 s52, s38, 0x100
	v_mov_b32_e32 v54, 0
	s_addc_u32 s53, s39, 0
	v_lshl_add_u64 v[2:3], s[16:17], 0, v[64:65]
	v_lshl_add_u64 v[74:75], s[16:17], 0, v[60:61]
	s_mov_b32 s54, -2
	s_mov_b64 s[38:39], 0
	v_mov_b32_e32 v55, v54
	v_mov_b32_e32 v56, v54
	v_mov_b32_e32 v57, v54
	v_mov_b32_e32 v70, v54
	v_mov_b32_e32 v71, v54
	v_mov_b32_e32 v72, v54
	v_mov_b32_e32 v73, v54
	v_mov_b32_e32 v86, v54
	v_mov_b32_e32 v87, v54
	v_mov_b32_e32 v88, v54
	v_mov_b32_e32 v89, v54
	v_mov_b32_e32 v94, v54
	v_mov_b32_e32 v95, v54
	v_mov_b32_e32 v96, v54
	v_mov_b32_e32 v97, v54
	v_mov_b32_e32 v104, v54
	v_mov_b32_e32 v105, v54
	v_mov_b32_e32 v106, v54
	v_mov_b32_e32 v107, v54
	v_mov_b32_e32 v112, v54
	v_mov_b32_e32 v113, v54
	v_mov_b32_e32 v114, v54
	v_mov_b32_e32 v115, v54
	v_mov_b32_e32 v120, v54
	v_mov_b32_e32 v121, v54
	v_mov_b32_e32 v122, v54
	v_mov_b32_e32 v123, v54
	v_mov_b32_e32 v128, v54
	v_mov_b32_e32 v129, v54
	v_mov_b32_e32 v130, v54
	v_mov_b32_e32 v131, v54
	v_mov_b32_e32 v140, v54
	v_mov_b32_e32 v141, v54
	v_mov_b32_e32 v142, v54
	v_mov_b32_e32 v143, v54
	v_mov_b32_e32 v148, v54
	v_mov_b32_e32 v149, v54
	v_mov_b32_e32 v150, v54
	v_mov_b32_e32 v151, v54
	v_mov_b32_e32 v90, v54
	v_mov_b32_e32 v91, v54
	v_mov_b32_e32 v92, v54
	v_mov_b32_e32 v93, v54
	v_mov_b32_e32 v100, v54
	v_mov_b32_e32 v101, v54
	v_mov_b32_e32 v102, v54
	v_mov_b32_e32 v103, v54
	v_mov_b32_e32 v108, v54
	v_mov_b32_e32 v109, v54
	v_mov_b32_e32 v110, v54
	v_mov_b32_e32 v111, v54
	v_mov_b32_e32 v116, v54
	v_mov_b32_e32 v117, v54
	v_mov_b32_e32 v118, v54
	v_mov_b32_e32 v119, v54
	v_mov_b32_e32 v124, v54
	v_mov_b32_e32 v125, v54
	v_mov_b32_e32 v126, v54
	v_mov_b32_e32 v127, v54
	v_mov_b32_e32 v132, v54
	v_mov_b32_e32 v133, v54
	v_mov_b32_e32 v134, v54
	v_mov_b32_e32 v135, v54
	v_mov_b32_e32 v144, v54
	v_mov_b32_e32 v145, v54
	v_mov_b32_e32 v146, v54
	v_mov_b32_e32 v147, v54
	v_mov_b32_e32 v152, v54
	v_mov_b32_e32 v153, v54
	v_mov_b32_e32 v154, v54
	v_mov_b32_e32 v155, v54
	v_mov_b32_e32 v46, v54
	v_mov_b32_e32 v47, v54
	v_mov_b32_e32 v48, v54
	v_mov_b32_e32 v49, v54
	v_mov_b32_e32 v38, v54
	v_mov_b32_e32 v39, v54
	v_mov_b32_e32 v40, v54
	v_mov_b32_e32 v41, v54
	v_mov_b32_e32 v30, v54
	v_mov_b32_e32 v31, v54
	v_mov_b32_e32 v32, v54
	v_mov_b32_e32 v33, v54
	v_mov_b32_e32 v22, v54
	v_mov_b32_e32 v23, v54
	v_mov_b32_e32 v24, v54
	v_mov_b32_e32 v25, v54
	v_mov_b32_e32 v14, v54
	v_mov_b32_e32 v15, v54
	v_mov_b32_e32 v16, v54
	v_mov_b32_e32 v17, v54
	v_mov_b32_e32 v6, v54
	v_mov_b32_e32 v7, v54
	v_mov_b32_e32 v8, v54
	v_mov_b32_e32 v9, v54
	v_mov_b32_e32 v82, v54
	v_mov_b32_e32 v83, v54
	v_mov_b32_e32 v84, v54
	v_mov_b32_e32 v85, v54
	v_mov_b32_e32 v66, v54
	v_mov_b32_e32 v67, v54
	v_mov_b32_e32 v68, v54
	v_mov_b32_e32 v69, v54
	v_mov_b32_e32 v50, v54
	v_mov_b32_e32 v51, v54
	v_mov_b32_e32 v52, v54
	v_mov_b32_e32 v53, v54
	v_mov_b32_e32 v42, v54
	v_mov_b32_e32 v43, v54
	v_mov_b32_e32 v44, v54
	v_mov_b32_e32 v45, v54
	v_mov_b32_e32 v34, v54
	v_mov_b32_e32 v35, v54
	v_mov_b32_e32 v36, v54
	v_mov_b32_e32 v37, v54
	v_mov_b32_e32 v26, v54
	v_mov_b32_e32 v27, v54
	v_mov_b32_e32 v28, v54
	v_mov_b32_e32 v29, v54
	v_mov_b32_e32 v18, v54
	v_mov_b32_e32 v19, v54
	v_mov_b32_e32 v20, v54
	v_mov_b32_e32 v21, v54
	v_mov_b32_e32 v10, v54
	v_mov_b32_e32 v11, v54
	v_mov_b32_e32 v12, v54
	v_mov_b32_e32 v13, v54
	.p2alignl 6, 3212836864

.LBB0_2957:
	s_ashr_i32 s35, s16, 31
	s_mov_b32 s34, s16
	s_lshl_b64 s[34:35], s[34:35], 19
	s_add_u32 s34, s27, s34
	s_addc_u32 s35, s49, s35
	s_ashr_i32 s37, s17, 31
	s_mov_b32 s36, s17
	s_lshl_b64 s[36:37], s[36:37], 19
	s_add_u32 s36, s25, s36
	s_addc_u32 s37, s26, s37
	s_and_b64 s[42:43], s[18:19], exec
	s_cselect_b32 s57, s37, s41
	s_cselect_b32 s64, s36, s40
	s_add_u32 s65, s40, 0x100
	s_addc_u32 s76, s41, 0
	s_add_u32 s40, s38, 0x40080
	s_addc_u32 s41, s39, 0
	v_mov_b32_e32 v6, 0
	v_lshl_add_u64 v[2:3], s[40:41], 0, v[158:159]
	s_waitcnt vmcnt(0)
	v_lshl_add_u64 v[140:141], s[40:41], 0, v[160:161]
	s_mov_b32 s78, -2
	s_mov_b64 s[40:41], 0
	v_mov_b32_e32 v7, v6
	v_mov_b32_e32 v8, v6
	v_mov_b32_e32 v9, v6
	v_mov_b32_e32 v10, v6
	v_mov_b32_e32 v11, v6
	v_mov_b32_e32 v12, v6
	v_mov_b32_e32 v13, v6
	v_mov_b32_e32 v24, v6
	v_mov_b32_e32 v25, v6
	v_mov_b32_e32 v26, v6
	v_mov_b32_e32 v27, v6
	v_mov_b32_e32 v28, v6
	v_mov_b32_e32 v29, v6
	v_mov_b32_e32 v30, v6
	v_mov_b32_e32 v31, v6
	v_mov_b32_e32 v40, v6
	v_mov_b32_e32 v41, v6
	v_mov_b32_e32 v42, v6
	v_mov_b32_e32 v43, v6
	v_mov_b32_e32 v44, v6
	v_mov_b32_e32 v45, v6
	v_mov_b32_e32 v46, v6
	v_mov_b32_e32 v47, v6
	v_mov_b32_e32 v56, v6
	v_mov_b32_e32 v57, v6
	v_mov_b32_e32 v58, v6
	v_mov_b32_e32 v59, v6
	v_mov_b32_e32 v60, v6
	v_mov_b32_e32 v61, v6
	v_mov_b32_e32 v62, v6
	v_mov_b32_e32 v63, v6
	v_mov_b32_e32 v14, v6
	v_mov_b32_e32 v15, v6
	v_mov_b32_e32 v16, v6
	v_mov_b32_e32 v17, v6
	v_mov_b32_e32 v18, v6
	v_mov_b32_e32 v19, v6
	v_mov_b32_e32 v20, v6
	v_mov_b32_e32 v21, v6
	v_mov_b32_e32 v32, v6
	v_mov_b32_e32 v33, v6
	v_mov_b32_e32 v34, v6
	v_mov_b32_e32 v35, v6
	v_mov_b32_e32 v36, v6
	v_mov_b32_e32 v37, v6
	v_mov_b32_e32 v38, v6
	v_mov_b32_e32 v39, v6
	v_mov_b32_e32 v48, v6
	v_mov_b32_e32 v49, v6
	v_mov_b32_e32 v50, v6
	v_mov_b32_e32 v51, v6
	v_mov_b32_e32 v52, v6
	v_mov_b32_e32 v53, v6
	v_mov_b32_e32 v54, v6
	v_mov_b32_e32 v55, v6
	v_mov_b32_e32 v64, v6
	v_mov_b32_e32 v65, v6
	v_mov_b32_e32 v66, v6
	v_mov_b32_e32 v67, v6
	v_mov_b32_e32 v68, v6
	v_mov_b32_e32 v69, v6
	v_mov_b32_e32 v70, v6
	v_mov_b32_e32 v71, v6
	v_mov_b32_e32 v72, v6
	v_mov_b32_e32 v73, v6
	v_mov_b32_e32 v74, v6
	v_mov_b32_e32 v75, v6
	v_mov_b32_e32 v76, v6
	v_mov_b32_e32 v77, v6
	v_mov_b32_e32 v78, v6
	v_mov_b32_e32 v79, v6
	v_mov_b32_e32 v88, v6
	v_mov_b32_e32 v89, v6
	v_mov_b32_e32 v90, v6
	v_mov_b32_e32 v91, v6
	v_mov_b32_e32 v92, v6
	v_mov_b32_e32 v93, v6
	v_mov_b32_e32 v94, v6
	v_mov_b32_e32 v95, v6
	v_mov_b32_e32 v108, v6
	v_mov_b32_e32 v109, v6
	v_mov_b32_e32 v110, v6
	v_mov_b32_e32 v111, v6
	v_mov_b32_e32 v112, v6
	v_mov_b32_e32 v113, v6
	v_mov_b32_e32 v114, v6
	v_mov_b32_e32 v115, v6
	v_mov_b32_e32 v124, v6
	v_mov_b32_e32 v125, v6
	v_mov_b32_e32 v126, v6
	v_mov_b32_e32 v127, v6
	v_mov_b32_e32 v128, v6
	v_mov_b32_e32 v129, v6
	v_mov_b32_e32 v130, v6
	v_mov_b32_e32 v131, v6
	v_mov_b32_e32 v80, v6
	v_mov_b32_e32 v81, v6
	v_mov_b32_e32 v82, v6
	v_mov_b32_e32 v83, v6
	v_mov_b32_e32 v84, v6
	v_mov_b32_e32 v85, v6
	v_mov_b32_e32 v86, v6
	v_mov_b32_e32 v87, v6
	v_mov_b32_e32 v100, v6
	v_mov_b32_e32 v101, v6
	v_mov_b32_e32 v102, v6
	v_mov_b32_e32 v103, v6
	v_mov_b32_e32 v104, v6
	v_mov_b32_e32 v105, v6
	v_mov_b32_e32 v106, v6
	v_mov_b32_e32 v107, v6
	v_mov_b32_e32 v116, v6
	v_mov_b32_e32 v117, v6
	v_mov_b32_e32 v118, v6
	v_mov_b32_e32 v119, v6
	v_mov_b32_e32 v120, v6
	v_mov_b32_e32 v121, v6
	v_mov_b32_e32 v122, v6
	v_mov_b32_e32 v123, v6
	v_mov_b32_e32 v132, v6
	v_mov_b32_e32 v133, v6
	v_mov_b32_e32 v134, v6
	v_mov_b32_e32 v135, v6
	v_mov_b32_e32 v136, v6
	v_mov_b32_e32 v137, v6
	v_mov_b32_e32 v138, v6
	v_mov_b32_e32 v139, v6
	.p2alignl 6, 3212836864

.LBB0_2961:
	v_ashrrev_i32_e32 v3, 31, v22
	v_mov_b32_e32 v2, v22
	v_lshlrev_b64 v[2:3], 12, v[2:3]
	v_lshl_add_u64 v[140:141], s[8:9], 0, v[2:3]
	v_lshl_or_b32 v2, v23, 8, v164
	v_ashrrev_i32_e32 v3, 31, v2
	v_lshl_add_u64 v[22:23], v[2:3], 2, v[140:141]
	global_load_dwordx4 v[148:151], v[22:23], off offset:16
	global_load_dwordx4 v[152:155], v[22:23], off
	global_load_dwordx4 v[140:143], v[22:23], off offset:528
	global_load_dwordx4 v[144:147], v[22:23], off offset:512
	s_lshl_b32 s22, s31, 10
	v_add_u32_e32 v22, s22, v163
	ds_read_b32 v98, v22
	s_waitcnt lgkmcnt(0)
	v_cmp_lt_i32_e32 vcc, -1, v98
	s_and_saveexec_b64 s[38:39], vcc
	s_cbranch_execz .LBB0_2963
	v_lshl_add_u64 v[166:167], v[98:99], 2, s[10:11]
	global_load_dword v166, v[166:167], off
	v_lshlrev_b64 v[168:169], 11, v[98:99]
	s_waitcnt vmcnt(0)
	v_pk_add_f32 v[138:139], v[138:139], v[154:155]
	v_pk_add_f32 v[136:137], v[136:137], v[152:153]
	v_pk_add_f32 v[134:135], v[134:135], v[150:151]
	v_pk_add_f32 v[132:133], v[132:133], v[148:149]
	v_pk_add_f32 v[130:131], v[130:131], v[146:147]
	v_pk_add_f32 v[128:129], v[128:129], v[144:145]
	v_pk_add_f32 v[126:127], v[126:127], v[142:143]
	v_pk_add_f32 v[124:125], v[124:125], v[140:141]
	v_lshl_add_u64 v[168:169], s[12:13], 0, v[168:169]
	v_lshl_add_u64 v[168:169], v[2:3], 1, v[168:169]
	v_pk_mul_f32 v[138:139], v[138:139], v[166:167] op_sel_hi:[1,0]
	v_pk_mul_f32 v[136:137], v[136:137], v[166:167] op_sel_hi:[1,0]
	v_pk_mul_f32 v[134:135], v[134:135], v[166:167] op_sel_hi:[1,0]
	v_pk_mul_f32 v[132:133], v[132:133], v[166:167] op_sel_hi:[1,0]
	v_pk_mul_f32 v[130:131], v[130:131], v[166:167] op_sel_hi:[1,0]
	v_pk_mul_f32 v[128:129], v[128:129], v[166:167] op_sel_hi:[1,0]
	v_pk_mul_f32 v[170:171], v[126:127], v[166:167] op_sel_hi:[1,0]
	v_pk_mul_f32 v[166:167], v[124:125], v[166:167] op_sel_hi:[1,0]
	v_cvt_pk_bf16_f32 v124, v136, v137
	v_cvt_pk_bf16_f32 v125, v138, v139
	v_cvt_pk_bf16_f32 v126, v132, v133
	v_cvt_pk_bf16_f32 v127, v134, v135
	v_cvt_pk_bf16_f32 v128, v128, v129
	v_cvt_pk_bf16_f32 v129, v130, v131
	v_cvt_pk_bf16_f32 v130, v166, v167
	v_cvt_pk_bf16_f32 v131, v170, v171
	global_store_dwordx4 v[168:169], v[124:127], off
	global_store_dwordx4 v[168:169], v[128:131], off offset:256
.LBB0_2963:
	s_or_b64 exec, exec, s[38:39]
	ds_read_b32 v98, v22 offset:64
	s_waitcnt lgkmcnt(0)
	v_cmp_lt_i32_e32 vcc, -1, v98
	s_and_saveexec_b64 s[38:39], vcc
	s_cbranch_execz .LBB0_2965
	v_lshl_add_u64 v[124:125], v[98:99], 2, s[10:11]
	global_load_dword v124, v[124:125], off
	v_lshlrev_b64 v[126:127], 11, v[98:99]
	s_waitcnt vmcnt(0)
	v_pk_add_f32 v[122:123], v[122:123], v[154:155]
	v_pk_add_f32 v[120:121], v[120:121], v[152:153]
	v_pk_add_f32 v[118:119], v[118:119], v[150:151]
	v_pk_add_f32 v[116:117], v[116:117], v[148:149]
	v_pk_add_f32 v[114:115], v[114:115], v[146:147]
	v_pk_add_f32 v[112:113], v[112:113], v[144:145]
	v_pk_add_f32 v[110:111], v[110:111], v[142:143]
	v_pk_add_f32 v[108:109], v[108:109], v[140:141]
	v_lshl_add_u64 v[126:127], s[12:13], 0, v[126:127]
	v_lshl_add_u64 v[126:127], v[2:3], 1, v[126:127]
	v_pk_mul_f32 v[122:123], v[122:123], v[124:125] op_sel_hi:[1,0]
	v_pk_mul_f32 v[120:121], v[120:121], v[124:125] op_sel_hi:[1,0]
	v_pk_mul_f32 v[118:119], v[118:119], v[124:125] op_sel_hi:[1,0]
	v_pk_mul_f32 v[116:117], v[116:117], v[124:125] op_sel_hi:[1,0]
	v_pk_mul_f32 v[114:115], v[114:115], v[124:125] op_sel_hi:[1,0]
	v_pk_mul_f32 v[112:113], v[112:113], v[124:125] op_sel_hi:[1,0]
	v_pk_mul_f32 v[128:129], v[110:111], v[124:125] op_sel_hi:[1,0]
	v_pk_mul_f32 v[124:125], v[108:109], v[124:125] op_sel_hi:[1,0]
	v_cvt_pk_bf16_f32 v108, v120, v121
	v_cvt_pk_bf16_f32 v109, v122, v123
	v_cvt_pk_bf16_f32 v110, v116, v117
	v_cvt_pk_bf16_f32 v111, v118, v119
	v_cvt_pk_bf16_f32 v112, v112, v113
	v_cvt_pk_bf16_f32 v113, v114, v115
	v_cvt_pk_bf16_f32 v114, v124, v125
	v_cvt_pk_bf16_f32 v115, v128, v129
	global_store_dwordx4 v[126:127], v[108:111], off
	global_store_dwordx4 v[126:127], v[112:115], off offset:256
.LBB0_2965:
	s_or_b64 exec, exec, s[38:39]
	ds_read_b32 v98, v22 offset:128
	s_waitcnt lgkmcnt(0)
	v_cmp_lt_i32_e32 vcc, -1, v98
	s_and_saveexec_b64 s[38:39], vcc
	s_cbranch_execz .LBB0_2967
	v_lshl_add_u64 v[108:109], v[98:99], 2, s[10:11]
	global_load_dword v108, v[108:109], off
	v_lshlrev_b64 v[110:111], 11, v[98:99]
	s_waitcnt vmcnt(0)
	v_pk_add_f32 v[106:107], v[106:107], v[154:155]
	v_pk_add_f32 v[104:105], v[104:105], v[152:153]
	v_pk_add_f32 v[102:103], v[102:103], v[150:151]
	v_pk_add_f32 v[100:101], v[100:101], v[148:149]
	v_pk_add_f32 v[94:95], v[94:95], v[146:147]
	v_pk_add_f32 v[92:93], v[92:93], v[144:145]
	v_pk_add_f32 v[90:91], v[90:91], v[142:143]
	v_pk_add_f32 v[88:89], v[88:89], v[140:141]
	v_lshl_add_u64 v[110:111], s[12:13], 0, v[110:111]
	v_lshl_add_u64 v[110:111], v[2:3], 1, v[110:111]
	v_pk_mul_f32 v[106:107], v[106:107], v[108:109] op_sel_hi:[1,0]
	v_pk_mul_f32 v[104:105], v[104:105], v[108:109] op_sel_hi:[1,0]
	v_pk_mul_f32 v[102:103], v[102:103], v[108:109] op_sel_hi:[1,0]
	v_pk_mul_f32 v[100:101], v[100:101], v[108:109] op_sel_hi:[1,0]
	v_pk_mul_f32 v[94:95], v[94:95], v[108:109] op_sel_hi:[1,0]
	v_pk_mul_f32 v[92:93], v[92:93], v[108:109] op_sel_hi:[1,0]
	v_pk_mul_f32 v[112:113], v[90:91], v[108:109] op_sel_hi:[1,0]
	v_pk_mul_f32 v[108:109], v[88:89], v[108:109] op_sel_hi:[1,0]
	v_cvt_pk_bf16_f32 v88, v104, v105
	v_cvt_pk_bf16_f32 v89, v106, v107
	v_cvt_pk_bf16_f32 v90, v100, v101
	v_cvt_pk_bf16_f32 v91, v102, v103
	v_cvt_pk_bf16_f32 v92, v92, v93
	v_cvt_pk_bf16_f32 v93, v94, v95
	v_cvt_pk_bf16_f32 v94, v108, v109
	v_cvt_pk_bf16_f32 v95, v112, v113
	global_store_dwordx4 v[110:111], v[88:91], off
	global_store_dwordx4 v[110:111], v[92:95], off offset:256
.LBB0_2967:
	s_or_b64 exec, exec, s[38:39]
	ds_read_b32 v98, v22 offset:192
	s_waitcnt lgkmcnt(0)
	v_cmp_lt_i32_e32 vcc, -1, v98
	s_and_saveexec_b64 s[38:39], vcc
	s_cbranch_execz .LBB0_2969
	v_lshl_add_u64 v[88:89], v[98:99], 2, s[10:11]
	global_load_dword v88, v[88:89], off
	v_lshlrev_b64 v[90:91], 11, v[98:99]
	s_waitcnt vmcnt(0)
	v_pk_add_f32 v[86:87], v[86:87], v[154:155]
	v_pk_add_f32 v[84:85], v[84:85], v[152:153]
	v_pk_add_f32 v[82:83], v[82:83], v[150:151]
	v_pk_add_f32 v[80:81], v[80:81], v[148:149]
	v_pk_add_f32 v[78:79], v[78:79], v[146:147]
	v_pk_add_f32 v[76:77], v[76:77], v[144:145]
	v_pk_add_f32 v[74:75], v[74:75], v[142:143]
	v_pk_add_f32 v[72:73], v[72:73], v[140:141]
	v_lshl_add_u64 v[90:91], s[12:13], 0, v[90:91]
	v_lshl_add_u64 v[90:91], v[2:3], 1, v[90:91]
	v_pk_mul_f32 v[86:87], v[86:87], v[88:89] op_sel_hi:[1,0]
	v_pk_mul_f32 v[84:85], v[84:85], v[88:89] op_sel_hi:[1,0]
	v_pk_mul_f32 v[82:83], v[82:83], v[88:89] op_sel_hi:[1,0]
	v_pk_mul_f32 v[80:81], v[80:81], v[88:89] op_sel_hi:[1,0]
	v_pk_mul_f32 v[78:79], v[78:79], v[88:89] op_sel_hi:[1,0]
	v_pk_mul_f32 v[76:77], v[76:77], v[88:89] op_sel_hi:[1,0]
	v_pk_mul_f32 v[92:93], v[74:75], v[88:89] op_sel_hi:[1,0]
	v_pk_mul_f32 v[88:89], v[72:73], v[88:89] op_sel_hi:[1,0]
	v_cvt_pk_bf16_f32 v72, v84, v85
	v_cvt_pk_bf16_f32 v73, v86, v87
	v_cvt_pk_bf16_f32 v74, v80, v81
	v_cvt_pk_bf16_f32 v75, v82, v83
	v_cvt_pk_bf16_f32 v76, v76, v77
	v_cvt_pk_bf16_f32 v77, v78, v79
	v_cvt_pk_bf16_f32 v78, v88, v89
	v_cvt_pk_bf16_f32 v79, v92, v93
	global_store_dwordx4 v[90:91], v[72:75], off
	global_store_dwordx4 v[90:91], v[76:79], off offset:256
.LBB0_2969:
	s_or_b64 exec, exec, s[38:39]
	ds_read_b32 v98, v22 offset:512
	s_waitcnt lgkmcnt(0)
	v_cmp_lt_i32_e32 vcc, -1, v98
	s_and_saveexec_b64 s[38:39], vcc
	s_cbranch_execz .LBB0_2971
	v_lshl_add_u64 v[72:73], v[98:99], 2, s[10:11]
	global_load_dword v72, v[72:73], off
	v_lshlrev_b64 v[74:75], 11, v[98:99]
	s_waitcnt vmcnt(0)
	v_pk_add_f32 v[70:71], v[70:71], v[154:155]
	v_pk_add_f32 v[68:69], v[68:69], v[152:153]
	v_pk_add_f32 v[66:67], v[66:67], v[150:151]
	v_pk_add_f32 v[64:65], v[64:65], v[148:149]
	v_pk_add_f32 v[62:63], v[62:63], v[146:147]
	v_pk_add_f32 v[60:61], v[60:61], v[144:145]
	v_pk_add_f32 v[58:59], v[58:59], v[142:143]
	v_pk_add_f32 v[56:57], v[56:57], v[140:141]
	v_lshl_add_u64 v[74:75], s[12:13], 0, v[74:75]
	v_lshl_add_u64 v[74:75], v[2:3], 1, v[74:75]
	v_pk_mul_f32 v[70:71], v[70:71], v[72:73] op_sel_hi:[1,0]
	v_pk_mul_f32 v[68:69], v[68:69], v[72:73] op_sel_hi:[1,0]
	v_pk_mul_f32 v[66:67], v[66:67], v[72:73] op_sel_hi:[1,0]
	v_pk_mul_f32 v[64:65], v[64:65], v[72:73] op_sel_hi:[1,0]
	v_pk_mul_f32 v[62:63], v[62:63], v[72:73] op_sel_hi:[1,0]
	v_pk_mul_f32 v[60:61], v[60:61], v[72:73] op_sel_hi:[1,0]
	v_pk_mul_f32 v[76:77], v[58:59], v[72:73] op_sel_hi:[1,0]
	v_pk_mul_f32 v[72:73], v[56:57], v[72:73] op_sel_hi:[1,0]
	v_cvt_pk_bf16_f32 v56, v68, v69
	v_cvt_pk_bf16_f32 v57, v70, v71
	v_cvt_pk_bf16_f32 v58, v64, v65
	v_cvt_pk_bf16_f32 v59, v66, v67
	v_cvt_pk_bf16_f32 v60, v60, v61
	v_cvt_pk_bf16_f32 v61, v62, v63
	v_cvt_pk_bf16_f32 v62, v72, v73
	v_cvt_pk_bf16_f32 v63, v76, v77
	global_store_dwordx4 v[74:75], v[56:59], off
	global_store_dwordx4 v[74:75], v[60:63], off offset:256
.LBB0_2971:
	s_or_b64 exec, exec, s[38:39]
	ds_read_b32 v98, v22 offset:576
	s_waitcnt lgkmcnt(0)
	v_cmp_lt_i32_e32 vcc, -1, v98
	s_and_saveexec_b64 s[38:39], vcc
	s_cbranch_execz .LBB0_2973
	v_lshl_add_u64 v[56:57], v[98:99], 2, s[10:11]
	global_load_dword v56, v[56:57], off
	v_lshlrev_b64 v[58:59], 11, v[98:99]
	s_waitcnt vmcnt(0)
	v_pk_add_f32 v[54:55], v[54:55], v[154:155]
	v_pk_add_f32 v[52:53], v[52:53], v[152:153]
	v_pk_add_f32 v[50:51], v[50:51], v[150:151]
	v_pk_add_f32 v[48:49], v[48:49], v[148:149]
	v_pk_add_f32 v[46:47], v[46:47], v[146:147]
	v_pk_add_f32 v[44:45], v[44:45], v[144:145]
	v_pk_add_f32 v[42:43], v[42:43], v[142:143]
	v_pk_add_f32 v[40:41], v[40:41], v[140:141]
	v_lshl_add_u64 v[58:59], s[12:13], 0, v[58:59]
	v_lshl_add_u64 v[58:59], v[2:3], 1, v[58:59]
	v_pk_mul_f32 v[54:55], v[54:55], v[56:57] op_sel_hi:[1,0]
	v_pk_mul_f32 v[52:53], v[52:53], v[56:57] op_sel_hi:[1,0]
	v_pk_mul_f32 v[50:51], v[50:51], v[56:57] op_sel_hi:[1,0]
	v_pk_mul_f32 v[48:49], v[48:49], v[56:57] op_sel_hi:[1,0]
	v_pk_mul_f32 v[46:47], v[46:47], v[56:57] op_sel_hi:[1,0]
	v_pk_mul_f32 v[44:45], v[44:45], v[56:57] op_sel_hi:[1,0]
	v_pk_mul_f32 v[60:61], v[42:43], v[56:57] op_sel_hi:[1,0]
	v_pk_mul_f32 v[56:57], v[40:41], v[56:57] op_sel_hi:[1,0]
	v_cvt_pk_bf16_f32 v40, v52, v53
	v_cvt_pk_bf16_f32 v41, v54, v55
	v_cvt_pk_bf16_f32 v42, v48, v49
	v_cvt_pk_bf16_f32 v43, v50, v51
	v_cvt_pk_bf16_f32 v44, v44, v45
	v_cvt_pk_bf16_f32 v45, v46, v47
	v_cvt_pk_bf16_f32 v46, v56, v57
	v_cvt_pk_bf16_f32 v47, v60, v61
	global_store_dwordx4 v[58:59], v[40:43], off
	global_store_dwordx4 v[58:59], v[44:47], off offset:256
.LBB0_2973:
	s_or_b64 exec, exec, s[38:39]
	ds_read_b32 v98, v22 offset:640
	s_waitcnt lgkmcnt(0)
	v_cmp_lt_i32_e32 vcc, -1, v98
	s_and_saveexec_b64 s[38:39], vcc
	s_cbranch_execz .LBB0_2975
	v_lshl_add_u64 v[40:41], v[98:99], 2, s[10:11]
	global_load_dword v40, v[40:41], off
	v_lshlrev_b64 v[42:43], 11, v[98:99]
	s_waitcnt vmcnt(0)
	v_pk_add_f32 v[38:39], v[38:39], v[154:155]
	v_pk_add_f32 v[36:37], v[36:37], v[152:153]
	v_pk_add_f32 v[34:35], v[34:35], v[150:151]
	v_pk_add_f32 v[32:33], v[32:33], v[148:149]
	v_pk_add_f32 v[30:31], v[30:31], v[146:147]
	v_pk_add_f32 v[28:29], v[28:29], v[144:145]
	v_pk_add_f32 v[26:27], v[26:27], v[142:143]
	v_pk_add_f32 v[24:25], v[24:25], v[140:141]
	v_lshl_add_u64 v[42:43], s[12:13], 0, v[42:43]
	v_lshl_add_u64 v[42:43], v[2:3], 1, v[42:43]
	v_pk_mul_f32 v[38:39], v[38:39], v[40:41] op_sel_hi:[1,0]
	v_pk_mul_f32 v[36:37], v[36:37], v[40:41] op_sel_hi:[1,0]
	v_pk_mul_f32 v[34:35], v[34:35], v[40:41] op_sel_hi:[1,0]
	v_pk_mul_f32 v[32:33], v[32:33], v[40:41] op_sel_hi:[1,0]
	v_pk_mul_f32 v[30:31], v[30:31], v[40:41] op_sel_hi:[1,0]
	v_pk_mul_f32 v[28:29], v[28:29], v[40:41] op_sel_hi:[1,0]
	v_pk_mul_f32 v[44:45], v[26:27], v[40:41] op_sel_hi:[1,0]
	v_pk_mul_f32 v[40:41], v[24:25], v[40:41] op_sel_hi:[1,0]
	v_cvt_pk_bf16_f32 v24, v36, v37
	v_cvt_pk_bf16_f32 v25, v38, v39
	v_cvt_pk_bf16_f32 v26, v32, v33
	v_cvt_pk_bf16_f32 v27, v34, v35
	v_cvt_pk_bf16_f32 v28, v28, v29
	v_cvt_pk_bf16_f32 v29, v30, v31
	v_cvt_pk_bf16_f32 v30, v40, v41
	v_cvt_pk_bf16_f32 v31, v44, v45
	global_store_dwordx4 v[42:43], v[24:27], off
	global_store_dwordx4 v[42:43], v[28:31], off offset:256
.LBB0_2975:
	s_or_b64 exec, exec, s[38:39]
	ds_read_b32 v98, v22 offset:704
	s_waitcnt lgkmcnt(0)
	v_cmp_lt_i32_e32 vcc, -1, v98
	s_and_saveexec_b64 s[38:39], vcc
	s_cbranch_execz .LBB0_2977
	v_lshl_add_u64 v[22:23], v[98:99], 2, s[10:11]
	global_load_dword v22, v[22:23], off
	v_lshlrev_b64 v[24:25], 11, v[98:99]
	s_waitcnt vmcnt(0)
	v_pk_add_f32 v[20:21], v[20:21], v[154:155]
	v_pk_add_f32 v[18:19], v[18:19], v[152:153]
	v_pk_add_f32 v[16:17], v[16:17], v[150:151]
	v_pk_add_f32 v[14:15], v[14:15], v[148:149]
	v_pk_add_f32 v[12:13], v[12:13], v[146:147]
	v_pk_add_f32 v[10:11], v[10:11], v[144:145]
	v_pk_add_f32 v[8:9], v[8:9], v[142:143]
	v_pk_add_f32 v[6:7], v[6:7], v[140:141]
	v_lshl_add_u64 v[24:25], s[12:13], 0, v[24:25]
	v_lshl_add_u64 v[2:3], v[2:3], 1, v[24:25]
	v_pk_mul_f32 v[20:21], v[20:21], v[22:23] op_sel_hi:[1,0]
	v_pk_mul_f32 v[18:19], v[18:19], v[22:23] op_sel_hi:[1,0]
	v_pk_mul_f32 v[16:17], v[16:17], v[22:23] op_sel_hi:[1,0]
	v_pk_mul_f32 v[14:15], v[14:15], v[22:23] op_sel_hi:[1,0]
	v_pk_mul_f32 v[12:13], v[12:13], v[22:23] op_sel_hi:[1,0]
	v_pk_mul_f32 v[10:11], v[10:11], v[22:23] op_sel_hi:[1,0]
	v_pk_mul_f32 v[24:25], v[8:9], v[22:23] op_sel_hi:[1,0]
	v_pk_mul_f32 v[22:23], v[6:7], v[22:23] op_sel_hi:[1,0]
	v_cvt_pk_bf16_f32 v6, v18, v19
	v_cvt_pk_bf16_f32 v7, v20, v21
	v_cvt_pk_bf16_f32 v8, v14, v15
	v_cvt_pk_bf16_f32 v9, v16, v17
	v_cvt_pk_bf16_f32 v10, v10, v11
	v_cvt_pk_bf16_f32 v11, v12, v13
	v_cvt_pk_bf16_f32 v12, v22, v23
	v_cvt_pk_bf16_f32 v13, v24, v25
	global_store_dwordx4 v[2:3], v[6:9], off
	global_store_dwordx4 v[2:3], v[10:13], off offset:256
